# baseline (speedup 1.0000x reference)
_Z6k_gemmIN2pg6EpiLinILi0EEELi768EEvNS0_4GemmET_:
	s_mov_b32 s77, 0
	s_load_dwordx2 s[4:5], s[0:1], 0x10
	v_readfirstlane_b32 s36, v0
	s_waitcnt lgkmcnt(0)
	s_ashr_i32 s3, s4, 31
	s_ashr_i32 s6, s5, 31
	s_lshr_b32 s3, s3, 24
	s_lshr_b32 s6, s6, 24
	s_add_i32 s3, s4, s3
	s_add_i32 s4, s5, s6
	s_ashr_i32 s3, s3, 8
	s_ashr_i32 s33, s4, 8
	s_mul_i32 s6, s33, s3
	s_cmp_ge_i32 s2, s6
	s_cbranch_scc1 .LBB7_32
	s_ashr_i32 s7, s6, 31
	s_lshr_b32 s4, s7, 29
	s_add_i32 s4, s6, s4
	s_ashr_i32 s37, s4, 3
	s_and_b32 s4, s4, -8
	s_ashr_i32 s39, s2, 31
	s_sub_i32 s38, s6, s4
	s_lshr_b32 s4, s39, 29
	s_add_i32 s10, s2, s4
	s_and_b32 s4, s10, -8
	s_sub_i32 s4, s2, s4
	s_add_i32 s40, s37, 1
	s_cmp_ge_i32 s4, s38
	s_mul_i32 s41, s40, s38
	s_cbranch_scc0 .LBB7_3
	s_sub_i32 s8, s4, s38
	s_mul_i32 s8, s8, s37
	s_add_i32 s11, s8, s41
	s_ashr_i32 s8, s10, 3
	s_cbranch_execz .LBB7_4
	s_branch .LBB7_5

.LBB7_27:
	ds_read_b128 v[128:131], v170
	ds_read_b128 v[132:135], v170 offset:1024
	ds_read_b128 v[136:139], v170 offset:2048
	ds_read_b128 v[140:143], v170 offset:3072
	s_add_u32 s30, s28, 0xfffd0080
	s_addc_u32 s31, s29, -1
	s_cmp_eq_u32 s73, 8
	s_cselect_b32 s35, s9, s31
	s_cselect_b32 s34, s8, s30
	s_cselect_b32 s31, s1, s72
	s_cselect_b32 s30, s0, s71
	v_lshl_add_u64 v[162:163], s[28:29], 0, v[152:153]
	s_add_i32 m0, s43, 0xc000
	ds_read_b128 v[158:161], v171
	ds_read_b128 v[176:179], v171 offset:1024
	ds_read_b128 v[180:183], v171 offset:2048
	ds_read_b128 v[184:187], v171 offset:3072
	ds_read_b128 v[188:191], v171 offset:4096
	ds_read_b128 v[192:195], v171 offset:5120
	ds_read_b128 v[196:199], v171 offset:6144
	ds_read_b128 v[200:203], v171 offset:7168
	global_load_lds_dwordx4 v[162:163], off
	v_lshl_add_u64 v[162:163], s[28:29], 0, v[154:155]
	s_add_i32 m0, s43, 0xe000
	s_nop 0
	global_load_lds_dwordx4 v[162:163], off
	s_waitcnt lgkmcnt(8)
	s_barrier
	s_waitcnt lgkmcnt(0)
	s_setprio 1
	s_waitcnt lgkmcnt(0)
	v_mfma_f32_16x16x32_f16 v[124:127], v[128:131], v[158:161], v[124:127]
	v_mfma_f32_16x16x32_f16 v[120:123], v[136:139], v[158:161], v[120:123]
	v_mfma_f32_16x16x32_f16 v[108:111], v[128:131], v[180:183], v[108:111]
	v_mfma_f32_16x16x32_f16 v[104:107], v[136:139], v[180:183], v[104:107]
	v_mfma_f32_16x16x32_f16 v[96:99], v[128:131], v[188:191], v[96:99]
	v_mfma_f32_16x16x32_f16 v[88:91], v[136:139], v[188:191], v[88:91]
	v_mfma_f32_16x16x32_f16 v[80:83], v[128:131], v[196:199], v[80:83]
	v_mfma_f32_16x16x32_f16 v[72:75], v[136:139], v[196:199], v[72:75]
	v_mfma_f32_16x16x32_f16 v[124:127], v[132:135], v[176:179], v[124:127]
	v_mfma_f32_16x16x32_f16 v[120:123], v[140:143], v[176:179], v[120:123]
	v_mfma_f32_16x16x32_f16 v[108:111], v[132:135], v[184:187], v[108:111]
	v_mfma_f32_16x16x32_f16 v[104:107], v[140:143], v[184:187], v[104:107]
	v_mfma_f32_16x16x32_f16 v[96:99], v[132:135], v[192:195], v[96:99]
	v_mfma_f32_16x16x32_f16 v[88:91], v[140:143], v[192:195], v[88:91]
	v_mfma_f32_16x16x32_f16 v[80:83], v[132:135], v[200:203], v[80:83]
	v_mfma_f32_16x16x32_f16 v[72:75], v[140:143], v[200:203], v[72:75]
	s_setprio 0
	s_barrier
	s_add_i32 s74, s65, s42
	v_lshl_add_u64 v[162:163], s[30:31], 0, v[146:147]
	s_mov_b32 m0, s74
	ds_read_b128 v[204:207], v172
	ds_read_b128 v[208:211], v172 offset:1024
	ds_read_b128 v[212:215], v172 offset:2048
	ds_read_b128 v[216:219], v172 offset:3072
	global_load_lds_dwordx4 v[162:163], off
	v_lshl_add_u64 v[220:221], s[30:31], 0, v[150:151]
	s_add_i32 m0, s74, 0x2000
	s_nop 0
	global_load_lds_dwordx4 v[220:221], off
	s_barrier
	s_waitcnt lgkmcnt(0)
	s_setprio 1
	s_waitcnt lgkmcnt(0)
	v_mfma_f32_16x16x32_f16 v[116:119], v[204:207], v[158:161], v[116:119]
	v_mfma_f32_16x16x32_f16 v[112:115], v[212:215], v[158:161], v[112:115]
	v_mfma_f32_16x16x32_f16 v[100:103], v[204:207], v[180:183], v[100:103]
	v_mfma_f32_16x16x32_f16 v[92:95], v[212:215], v[180:183], v[92:95]
	v_mfma_f32_16x16x32_f16 v[84:87], v[204:207], v[188:191], v[84:87]
	v_mfma_f32_16x16x32_f16 v[76:79], v[212:215], v[188:191], v[76:79]
	v_mfma_f32_16x16x32_f16 v[68:71], v[204:207], v[196:199], v[68:71]
	v_mfma_f32_16x16x32_f16 v[64:67], v[212:215], v[196:199], v[64:67]
	v_mfma_f32_16x16x32_f16 v[116:119], v[208:211], v[176:179], v[116:119]
	v_mfma_f32_16x16x32_f16 v[112:115], v[216:219], v[176:179], v[112:115]
	v_mfma_f32_16x16x32_f16 v[100:103], v[208:211], v[184:187], v[100:103]
	v_mfma_f32_16x16x32_f16 v[92:95], v[216:219], v[184:187], v[92:95]
	v_mfma_f32_16x16x32_f16 v[84:87], v[208:211], v[192:195], v[84:87]
	v_mfma_f32_16x16x32_f16 v[76:79], v[216:219], v[192:195], v[76:79]
	v_mfma_f32_16x16x32_f16 v[68:71], v[208:211], v[200:203], v[68:71]
	v_mfma_f32_16x16x32_f16 v[64:67], v[216:219], v[200:203], v[64:67]
	s_setprio 0
	s_mov_b32 m0, s43
	v_lshl_add_u64 v[222:223], s[34:35], 0, v[144:145]
	s_barrier
	ds_read_b128 v[158:161], v171 offset:16384
	ds_read_b128 v[176:179], v171 offset:17408
	ds_read_b128 v[180:183], v171 offset:18432
	ds_read_b128 v[184:187], v171 offset:19456
	ds_read_b128 v[188:191], v171 offset:20480
	ds_read_b128 v[192:195], v171 offset:21504
	ds_read_b128 v[196:199], v171 offset:22528
	ds_read_b128 v[200:203], v171 offset:23552
	global_load_lds_dwordx4 v[222:223], off
	v_lshl_add_u64 v[224:225], s[34:35], 0, v[148:149]
	s_mov_b32 m0, s44
	s_nop 0
	global_load_lds_dwordx4 v[224:225], off
	s_barrier
	s_waitcnt lgkmcnt(0)
	s_setprio 1
	s_waitcnt lgkmcnt(0)
	v_mfma_f32_16x16x32_f16 v[60:63], v[128:131], v[158:161], v[60:63]
	v_mfma_f32_16x16x32_f16 v[56:59], v[136:139], v[158:161], v[56:59]
	v_mfma_f32_16x16x32_f16 v[48:51], v[128:131], v[180:183], v[48:51]
	v_mfma_f32_16x16x32_f16 v[40:43], v[136:139], v[180:183], v[40:43]
	v_mfma_f32_16x16x32_f16 v[32:35], v[128:131], v[188:191], v[32:35]
	v_mfma_f32_16x16x32_f16 v[24:27], v[136:139], v[188:191], v[24:27]
	v_mfma_f32_16x16x32_f16 v[16:19], v[128:131], v[196:199], v[16:19]
	v_mfma_f32_16x16x32_f16 v[8:11], v[136:139], v[196:199], v[8:11]
	v_mfma_f32_16x16x32_f16 v[60:63], v[132:135], v[176:179], v[60:63]
	v_mfma_f32_16x16x32_f16 v[56:59], v[140:143], v[176:179], v[56:59]
	v_mfma_f32_16x16x32_f16 v[48:51], v[132:135], v[184:187], v[48:51]
	v_mfma_f32_16x16x32_f16 v[40:43], v[140:143], v[184:187], v[40:43]
	v_mfma_f32_16x16x32_f16 v[32:35], v[132:135], v[192:195], v[32:35]
	v_mfma_f32_16x16x32_f16 v[24:27], v[140:143], v[192:195], v[24:27]
	v_mfma_f32_16x16x32_f16 v[16:19], v[132:135], v[200:203], v[16:19]
	v_mfma_f32_16x16x32_f16 v[8:11], v[140:143], v[200:203], v[8:11]
	s_setprio 0
	s_barrier
	s_add_u32 s74, s30, 0xc000
	s_addc_u32 s75, s31, 0
	s_add_i32 s76, s66, s42
	v_lshl_add_u64 v[128:129], s[74:75], 0, v[146:147]
	s_mov_b32 m0, s76
	s_nop 0
	global_load_lds_dwordx4 v[128:129], off
	v_lshl_add_u64 v[128:129], s[74:75], 0, v[150:151]
	s_add_i32 m0, s76, 0x2000
	s_nop 0
	global_load_lds_dwordx4 v[128:129], off
	s_waitcnt vmcnt(6)
	s_cmp_eq_u32 s77, 0
	s_cbranch_scc1 .Ldef7_a
	s_mul_i32 s78, s10, 288
	buffer_store_dwordx4 v[226:229], v250, s[20:23], s78 offen nt
	s_mul_i32 s78, s10, 304
	buffer_store_dwordx4 v[230:233], v250, s[20:23], s78 offen nt
	s_mul_i32 s78, s10, 320
	buffer_store_dwordx4 v[234:237], v250, s[20:23], s78 offen nt
.Ldef7_a:
	s_barrier
	s_setprio 1
	v_mfma_f32_16x16x32_f16 v[52:55], v[204:207], v[158:161], v[52:55]
	v_mfma_f32_16x16x32_f16 v[44:47], v[212:215], v[158:161], v[44:47]
	v_mfma_f32_16x16x32_f16 v[36:39], v[204:207], v[180:183], v[36:39]
	v_mfma_f32_16x16x32_f16 v[28:31], v[212:215], v[180:183], v[28:31]
	v_mfma_f32_16x16x32_f16 v[20:23], v[204:207], v[188:191], v[20:23]
	v_mfma_f32_16x16x32_f16 v[12:15], v[212:215], v[188:191], v[12:15]
	v_mfma_f32_16x16x32_f16 v[4:7], v[204:207], v[196:199], v[4:7]
	v_mfma_f32_16x16x32_f16 v[0:3], v[212:215], v[196:199], v[0:3]
	v_mfma_f32_16x16x32_f16 v[52:55], v[208:211], v[176:179], v[52:55]
	v_mfma_f32_16x16x32_f16 v[44:47], v[216:219], v[176:179], v[44:47]
	v_mfma_f32_16x16x32_f16 v[36:39], v[208:211], v[184:187], v[36:39]
	v_mfma_f32_16x16x32_f16 v[28:31], v[216:219], v[184:187], v[28:31]
	v_mfma_f32_16x16x32_f16 v[20:23], v[208:211], v[192:195], v[20:23]
	v_mfma_f32_16x16x32_f16 v[12:15], v[216:219], v[192:195], v[12:15]
	v_mfma_f32_16x16x32_f16 v[4:7], v[208:211], v[200:203], v[4:7]
	v_mfma_f32_16x16x32_f16 v[0:3], v[216:219], v[200:203], v[0:3]
	s_setprio 0
	s_add_i32 s74, 0, 0x18000
	v_add_u32_e32 v140, s74, v166
	s_barrier
	ds_read_b128 v[128:131], v140
	ds_read_b128 v[132:135], v140 offset:1024
	ds_read_b128 v[136:139], v140 offset:2048
	ds_read_b128 v[140:143], v140 offset:3072
	s_add_u32 s34, s34, 0x30000
	s_addc_u32 s35, s35, 0
	s_mov_b32 m0, s45
	v_lshl_add_u64 v[204:205], s[34:35], 0, v[144:145]
	ds_read_b128 v[158:161], v171 offset:32768
	ds_read_b128 v[176:179], v171 offset:33792
	ds_read_b128 v[180:183], v171 offset:34816
	ds_read_b128 v[184:187], v171 offset:35840
	ds_read_b128 v[188:191], v171 offset:36864
	ds_read_b128 v[192:195], v171 offset:37888
	ds_read_b128 v[196:199], v171 offset:38912
	ds_read_b128 v[200:203], v171 offset:39936
	global_load_lds_dwordx4 v[204:205], off
	v_lshl_add_u64 v[204:205], s[34:35], 0, v[148:149]
	s_mov_b32 m0, s46
	s_nop 0
	global_load_lds_dwordx4 v[204:205], off
	s_cmp_eq_u32 s73, 8
	s_cbranch_scc0 .Lpf7_skip
	s_lshl_b32 s78, s70, 8
	s_add_i32 s78, s78, s48
	v_or_b32_e32 v252, s78, v165
	v_ashrrev_i32_e32 v253, 31, v252
	v_lshl_add_u64 v[252:253], v[252:253], 3, s[12:13]
	s_lshl_b32 s79, s67, 8
	s_or_b32 s79, s79, s51
	v_or_b32_e32 v254, s79, v164
	v_ashrrev_i32_e32 v255, 31, v254
	v_lshl_add_u64 v[254:255], v[254:255], 2, s[14:15]
	global_load_dword v226, v[252:253], off offset:4
	global_load_dword v227, v[252:253], off offset:132
	global_load_dword v228, v[252:253], off offset:260
	global_load_dword v229, v[252:253], off offset:388
	global_load_dword v230, v[252:253], off offset:1028
	global_load_dword v231, v[252:253], off offset:1156
	global_load_dword v232, v[252:253], off offset:1284
	global_load_dword v233, v[252:253], off offset:1412
	global_load_dwordx4 v[234:237], v[254:255], off
	global_load_dwordx4 v[238:241], v[254:255], off offset:16
	global_load_dwordx4 v[242:245], v[254:255], off offset:128
	global_load_dwordx4 v[246:249], v[254:255], off offset:144
.Lpf7_skip:
	s_waitcnt lgkmcnt(8)
	s_barrier
	s_waitcnt lgkmcnt(0)
	s_setprio 1
	s_waitcnt lgkmcnt(0)
	v_mfma_f32_16x16x32_f16 v[124:127], v[128:131], v[158:161], v[124:127]
	v_mfma_f32_16x16x32_f16 v[120:123], v[136:139], v[158:161], v[120:123]
	v_mfma_f32_16x16x32_f16 v[108:111], v[128:131], v[180:183], v[108:111]
	v_mfma_f32_16x16x32_f16 v[104:107], v[136:139], v[180:183], v[104:107]
	v_mfma_f32_16x16x32_f16 v[96:99], v[128:131], v[188:191], v[96:99]
	v_mfma_f32_16x16x32_f16 v[88:91], v[136:139], v[188:191], v[88:91]
	v_mfma_f32_16x16x32_f16 v[80:83], v[128:131], v[196:199], v[80:83]
	v_mfma_f32_16x16x32_f16 v[72:75], v[136:139], v[196:199], v[72:75]
	v_mfma_f32_16x16x32_f16 v[124:127], v[132:135], v[176:179], v[124:127]
	v_mfma_f32_16x16x32_f16 v[120:123], v[140:143], v[176:179], v[120:123]
	v_mfma_f32_16x16x32_f16 v[108:111], v[132:135], v[184:187], v[108:111]
	v_mfma_f32_16x16x32_f16 v[104:107], v[140:143], v[184:187], v[104:107]
	v_mfma_f32_16x16x32_f16 v[96:99], v[132:135], v[192:195], v[96:99]
	v_mfma_f32_16x16x32_f16 v[88:91], v[140:143], v[192:195], v[88:91]
	v_mfma_f32_16x16x32_f16 v[80:83], v[132:135], v[200:203], v[80:83]
	v_mfma_f32_16x16x32_f16 v[72:75], v[140:143], v[200:203], v[72:75]
	s_setprio 0
	s_barrier
	s_add_i32 s34, 0, 0x1c000
	s_add_i32 s35, s74, s42
	v_add_u32_e32 v175, s34, v166
	v_lshl_add_u64 v[162:163], v[162:163], 0, s[26:27]
	s_mov_b32 m0, s35
	ds_read_b128 v[204:207], v175
	ds_read_b128 v[208:211], v175 offset:1024
	ds_read_b128 v[212:215], v175 offset:2048
	ds_read_b128 v[216:219], v175 offset:3072
	global_load_lds_dwordx4 v[162:163], off
	v_lshl_add_u64 v[162:163], v[220:221], 0, s[26:27]
	s_add_i32 m0, s35, 0x2000
	s_nop 0
	global_load_lds_dwordx4 v[162:163], off
	s_barrier
	s_waitcnt lgkmcnt(0)
	s_setprio 1
	s_waitcnt lgkmcnt(0)
	v_mfma_f32_16x16x32_f16 v[116:119], v[204:207], v[158:161], v[116:119]
	v_mfma_f32_16x16x32_f16 v[112:115], v[212:215], v[158:161], v[112:115]
	v_mfma_f32_16x16x32_f16 v[100:103], v[204:207], v[180:183], v[100:103]
	v_mfma_f32_16x16x32_f16 v[92:95], v[212:215], v[180:183], v[92:95]
	v_mfma_f32_16x16x32_f16 v[84:87], v[204:207], v[188:191], v[84:87]
	v_mfma_f32_16x16x32_f16 v[76:79], v[212:215], v[188:191], v[76:79]
	v_mfma_f32_16x16x32_f16 v[68:71], v[204:207], v[196:199], v[68:71]
	v_mfma_f32_16x16x32_f16 v[64:67], v[212:215], v[196:199], v[64:67]
	v_mfma_f32_16x16x32_f16 v[116:119], v[208:211], v[176:179], v[116:119]
	v_mfma_f32_16x16x32_f16 v[112:115], v[216:219], v[176:179], v[112:115]
	v_mfma_f32_16x16x32_f16 v[100:103], v[208:211], v[184:187], v[100:103]
	v_mfma_f32_16x16x32_f16 v[92:95], v[216:219], v[184:187], v[92:95]
	v_mfma_f32_16x16x32_f16 v[84:87], v[208:211], v[192:195], v[84:87]
	v_mfma_f32_16x16x32_f16 v[76:79], v[216:219], v[192:195], v[76:79]
	v_mfma_f32_16x16x32_f16 v[68:71], v[208:211], v[200:203], v[68:71]
	v_mfma_f32_16x16x32_f16 v[64:67], v[216:219], v[200:203], v[64:67]
	s_setprio 0
	s_mov_b32 m0, s49
	v_lshl_add_u64 v[162:163], v[222:223], 0, s[26:27]
	s_barrier
	ds_read_b128 v[158:161], v171 offset:49152
	ds_read_b128 v[176:179], v171 offset:50176
	ds_read_b128 v[180:183], v171 offset:51200
	ds_read_b128 v[184:187], v171 offset:52224
	ds_read_b128 v[188:191], v171 offset:53248
	ds_read_b128 v[192:195], v171 offset:54272
	ds_read_b128 v[196:199], v171 offset:55296
	ds_read_b128 v[200:203], v171 offset:56320
	global_load_lds_dwordx4 v[162:163], off
	v_lshl_add_u64 v[162:163], v[224:225], 0, s[26:27]
	s_mov_b32 m0, s50
	s_nop 0
	global_load_lds_dwordx4 v[162:163], off
	s_barrier
	s_waitcnt lgkmcnt(0)
	s_setprio 1
	s_waitcnt lgkmcnt(0)
	v_mfma_f32_16x16x32_f16 v[60:63], v[128:131], v[158:161], v[60:63]
	v_mfma_f32_16x16x32_f16 v[56:59], v[136:139], v[158:161], v[56:59]
	v_mfma_f32_16x16x32_f16 v[48:51], v[128:131], v[180:183], v[48:51]
	v_mfma_f32_16x16x32_f16 v[40:43], v[136:139], v[180:183], v[40:43]
	v_mfma_f32_16x16x32_f16 v[32:35], v[128:131], v[188:191], v[32:35]
	v_mfma_f32_16x16x32_f16 v[24:27], v[136:139], v[188:191], v[24:27]
	v_mfma_f32_16x16x32_f16 v[16:19], v[128:131], v[196:199], v[16:19]
	v_mfma_f32_16x16x32_f16 v[8:11], v[136:139], v[196:199], v[8:11]
	v_mfma_f32_16x16x32_f16 v[60:63], v[132:135], v[176:179], v[60:63]
	v_mfma_f32_16x16x32_f16 v[56:59], v[140:143], v[176:179], v[56:59]
	v_mfma_f32_16x16x32_f16 v[48:51], v[132:135], v[184:187], v[48:51]
	v_mfma_f32_16x16x32_f16 v[40:43], v[140:143], v[184:187], v[40:43]
	v_mfma_f32_16x16x32_f16 v[32:35], v[132:135], v[192:195], v[32:35]
	v_mfma_f32_16x16x32_f16 v[24:27], v[140:143], v[192:195], v[24:27]
	v_mfma_f32_16x16x32_f16 v[16:19], v[132:135], v[200:203], v[16:19]
	v_mfma_f32_16x16x32_f16 v[8:11], v[140:143], v[200:203], v[8:11]
	s_setprio 0
	s_barrier
	s_add_u32 s30, s30, 0xc080
	s_addc_u32 s31, s31, 0
	s_add_i32 s34, s34, s42
	v_lshl_add_u64 v[128:129], s[30:31], 0, v[146:147]
	s_mov_b32 m0, s34
	s_nop 0
	global_load_lds_dwordx4 v[128:129], off
	v_lshl_add_u64 v[128:129], s[30:31], 0, v[150:151]
	s_add_i32 m0, s34, 0x2000
	s_nop 0
	global_load_lds_dwordx4 v[128:129], off
	s_cmp_eq_u32 s73, 8
	s_cbranch_scc1 .Lw87_last
	s_waitcnt vmcnt(6)
	s_branch .Lw87_j
.Lw87_last:
	s_waitcnt vmcnt(18)
.Lw87_j:
	s_cmp_eq_u32 s77, 0
	s_cbranch_scc1 .Ldef7_b
	s_mul_i32 s78, s10, 336
	buffer_store_dwordx4 v[238:241], v250, s[20:23], s78 offen nt
	s_mul_i32 s78, s10, 352
	buffer_store_dwordx4 v[242:245], v250, s[20:23], s78 offen nt
	s_mul_i32 s78, s10, 368
	buffer_store_dwordx4 v[246:249], v250, s[20:23], s78 offen nt
	s_mov_b32 s77, 0
.Ldef7_b:
	s_barrier
	s_setprio 1
	v_mfma_f32_16x16x32_f16 v[52:55], v[204:207], v[158:161], v[52:55]
	v_mfma_f32_16x16x32_f16 v[44:47], v[212:215], v[158:161], v[44:47]
	v_mfma_f32_16x16x32_f16 v[36:39], v[204:207], v[180:183], v[36:39]
	v_mfma_f32_16x16x32_f16 v[28:31], v[212:215], v[180:183], v[28:31]
	v_mfma_f32_16x16x32_f16 v[20:23], v[204:207], v[188:191], v[20:23]
	v_mfma_f32_16x16x32_f16 v[12:15], v[212:215], v[188:191], v[12:15]
	v_mfma_f32_16x16x32_f16 v[4:7], v[204:207], v[196:199], v[4:7]
	v_mfma_f32_16x16x32_f16 v[0:3], v[212:215], v[196:199], v[0:3]
	v_mfma_f32_16x16x32_f16 v[52:55], v[208:211], v[176:179], v[52:55]
	v_mfma_f32_16x16x32_f16 v[44:47], v[216:219], v[176:179], v[44:47]
	v_mfma_f32_16x16x32_f16 v[36:39], v[208:211], v[184:187], v[36:39]
	v_mfma_f32_16x16x32_f16 v[28:31], v[216:219], v[184:187], v[28:31]
	v_mfma_f32_16x16x32_f16 v[20:23], v[208:211], v[192:195], v[20:23]
	v_mfma_f32_16x16x32_f16 v[12:15], v[216:219], v[192:195], v[12:15]
	v_mfma_f32_16x16x32_f16 v[4:7], v[208:211], v[200:203], v[4:7]
	v_mfma_f32_16x16x32_f16 v[0:3], v[216:219], v[200:203], v[0:3]
	s_setprio 0
	s_add_i32 s73, s73, 2
	s_add_u32 s28, s28, 0x100
	s_addc_u32 s29, s29, 0
	s_add_u32 s71, s71, 0x100
	s_addc_u32 s72, s72, 0
	s_cmp_gt_u32 s73, 9
	s_barrier
	s_cbranch_scc0 .LBB7_27
	s_lshl_b32 s28, s70, 8
	s_add_i32 s28, s28, s48
	s_lshl_b32 s29, s67, 8
	s_or_b32 s29, s29, s51
	s_waitcnt vmcnt(6)
	v_pk_fma_f32 v[124:125], v[124:125], v[226:227], v[234:235] op_sel_hi:[1,0,1]
	v_pk_fma_f32 v[126:127], v[126:127], v[226:227], v[236:237] op_sel_hi:[1,0,1]
	v_pk_fma_f32 v[120:121], v[120:121], v[226:227], v[238:239] op_sel_hi:[1,0,1]
	v_pk_fma_f32 v[122:123], v[122:123], v[226:227], v[240:241] op_sel_hi:[1,0,1]
	v_cvt_pk_f16_f32 v124, v124, v125
	v_cvt_pk_f16_f32 v125, v126, v127
	v_cvt_pk_f16_f32 v126, v120, v121
	v_cvt_pk_f16_f32 v127, v122, v123
	v_add_u32_e32 v250, s28, v167
	v_mul_lo_u32 v250, v250, s10
	v_add_u32_e32 v250, s29, v250
	v_lshl_add_u32 v250, v250, 1, v168
	ds_write_b128 v173, v[124:127]
	v_pk_fma_f32 v[116:117], v[116:117], v[226:227], v[242:243] op_sel_hi:[1,0,1]
	v_pk_fma_f32 v[118:119], v[118:119], v[226:227], v[244:245] op_sel_hi:[1,0,1]
	v_pk_fma_f32 v[112:113], v[112:113], v[226:227], v[246:247] op_sel_hi:[1,0,1]
	v_pk_fma_f32 v[114:115], v[114:115], v[226:227], v[248:249] op_sel_hi:[1,0,1]
	v_cvt_pk_f16_f32 v116, v116, v117
	v_cvt_pk_f16_f32 v117, v118, v119
	v_cvt_pk_f16_f32 v118, v112, v113
	v_cvt_pk_f16_f32 v119, v114, v115
	ds_write_b128 v173, v[116:119] offset:64
	ds_read_b128 v[120:123], v174
	ds_read_b128 v[112:115], v174 offset:1152
	v_pk_fma_f32 v[108:109], v[108:109], v[226:227], v[234:235] op_sel:[0,1,0]
	v_pk_fma_f32 v[110:111], v[110:111], v[226:227], v[236:237] op_sel:[0,1,0]
	v_pk_fma_f32 v[104:105], v[104:105], v[226:227], v[238:239] op_sel:[0,1,0]
	v_pk_fma_f32 v[106:107], v[106:107], v[226:227], v[240:241] op_sel:[0,1,0]
	v_cvt_pk_f16_f32 v108, v108, v109
	v_cvt_pk_f16_f32 v109, v110, v111
	v_cvt_pk_f16_f32 v110, v104, v105
	v_cvt_pk_f16_f32 v111, v106, v107
	s_waitcnt lgkmcnt(0)
	s_mul_i32 s34, s10, 0
	buffer_store_dwordx4 v[120:123], v250, s[20:23], s34 offen nt
	s_mul_i32 s35, s10, 16
	buffer_store_dwordx4 v[112:115], v250, s[20:23], s35 offen nt
	ds_write_b128 v173, v[108:111]
	v_pk_fma_f32 v[100:101], v[100:101], v[226:227], v[242:243] op_sel:[0,1,0]
	v_pk_fma_f32 v[102:103], v[102:103], v[226:227], v[244:245] op_sel:[0,1,0]
	v_pk_fma_f32 v[92:93], v[92:93], v[226:227], v[246:247] op_sel:[0,1,0]
	v_pk_fma_f32 v[94:95], v[94:95], v[226:227], v[248:249] op_sel:[0,1,0]
	v_cvt_pk_f16_f32 v100, v100, v101
	v_cvt_pk_f16_f32 v101, v102, v103
	v_cvt_pk_f16_f32 v102, v92, v93
	v_cvt_pk_f16_f32 v103, v94, v95
	ds_write_b128 v173, v[100:103] offset:64
	ds_read_b128 v[124:127], v174
	ds_read_b128 v[116:119], v174 offset:1152
	v_pk_fma_f32 v[96:97], v[96:97], v[228:229], v[234:235] op_sel_hi:[1,0,1]
	v_pk_fma_f32 v[98:99], v[98:99], v[228:229], v[236:237] op_sel_hi:[1,0,1]
	v_pk_fma_f32 v[88:89], v[88:89], v[228:229], v[238:239] op_sel_hi:[1,0,1]
	v_pk_fma_f32 v[90:91], v[90:91], v[228:229], v[240:241] op_sel_hi:[1,0,1]
	v_cvt_pk_f16_f32 v96, v96, v97
	v_cvt_pk_f16_f32 v97, v98, v99
	v_cvt_pk_f16_f32 v98, v88, v89
	v_cvt_pk_f16_f32 v99, v90, v91
	s_waitcnt lgkmcnt(0)
	s_mul_i32 s34, s10, 32
	buffer_store_dwordx4 v[124:127], v250, s[20:23], s34 offen nt
	s_mul_i32 s35, s10, 48
	buffer_store_dwordx4 v[116:119], v250, s[20:23], s35 offen nt
	ds_write_b128 v173, v[96:99]
	v_pk_fma_f32 v[84:85], v[84:85], v[228:229], v[242:243] op_sel_hi:[1,0,1]
	v_pk_fma_f32 v[86:87], v[86:87], v[228:229], v[244:245] op_sel_hi:[1,0,1]
	v_pk_fma_f32 v[76:77], v[76:77], v[228:229], v[246:247] op_sel_hi:[1,0,1]
	v_pk_fma_f32 v[78:79], v[78:79], v[228:229], v[248:249] op_sel_hi:[1,0,1]
	v_cvt_pk_f16_f32 v84, v84, v85
	v_cvt_pk_f16_f32 v85, v86, v87
	v_cvt_pk_f16_f32 v86, v76, v77
	v_cvt_pk_f16_f32 v87, v78, v79
	ds_write_b128 v173, v[84:87] offset:64
	ds_read_b128 v[120:123], v174
	ds_read_b128 v[112:115], v174 offset:1152
	v_pk_fma_f32 v[80:81], v[80:81], v[228:229], v[234:235] op_sel:[0,1,0]
	v_pk_fma_f32 v[82:83], v[82:83], v[228:229], v[236:237] op_sel:[0,1,0]
	v_pk_fma_f32 v[72:73], v[72:73], v[228:229], v[238:239] op_sel:[0,1,0]
	v_pk_fma_f32 v[74:75], v[74:75], v[228:229], v[240:241] op_sel:[0,1,0]
	v_cvt_pk_f16_f32 v80, v80, v81
	v_cvt_pk_f16_f32 v81, v82, v83
	v_cvt_pk_f16_f32 v82, v72, v73
	v_cvt_pk_f16_f32 v83, v74, v75
	s_waitcnt lgkmcnt(0)
	s_mul_i32 s34, s10, 64
	buffer_store_dwordx4 v[120:123], v250, s[20:23], s34 offen nt
	s_mul_i32 s35, s10, 80
	buffer_store_dwordx4 v[112:115], v250, s[20:23], s35 offen nt
	ds_write_b128 v173, v[80:83]
	v_pk_fma_f32 v[68:69], v[68:69], v[228:229], v[242:243] op_sel:[0,1,0]
	v_pk_fma_f32 v[70:71], v[70:71], v[228:229], v[244:245] op_sel:[0,1,0]
	v_pk_fma_f32 v[64:65], v[64:65], v[228:229], v[246:247] op_sel:[0,1,0]
	v_pk_fma_f32 v[66:67], v[66:67], v[228:229], v[248:249] op_sel:[0,1,0]
	v_cvt_pk_f16_f32 v68, v68, v69
	v_cvt_pk_f16_f32 v69, v70, v71
	v_cvt_pk_f16_f32 v70, v64, v65
	v_cvt_pk_f16_f32 v71, v66, v67
	ds_write_b128 v173, v[68:71] offset:64
	ds_read_b128 v[104:107], v174
	ds_read_b128 v[92:95], v174 offset:1152
	v_pk_fma_f32 v[60:61], v[60:61], v[230:231], v[234:235] op_sel_hi:[1,0,1]
	v_pk_fma_f32 v[62:63], v[62:63], v[230:231], v[236:237] op_sel_hi:[1,0,1]
	v_pk_fma_f32 v[56:57], v[56:57], v[230:231], v[238:239] op_sel_hi:[1,0,1]
	v_pk_fma_f32 v[58:59], v[58:59], v[230:231], v[240:241] op_sel_hi:[1,0,1]
	v_cvt_pk_f16_f32 v60, v60, v61
	v_cvt_pk_f16_f32 v61, v62, v63
	v_cvt_pk_f16_f32 v62, v56, v57
	v_cvt_pk_f16_f32 v63, v58, v59
	s_waitcnt lgkmcnt(0)
	s_mul_i32 s34, s10, 96
	buffer_store_dwordx4 v[104:107], v250, s[20:23], s34 offen nt
	s_mul_i32 s35, s10, 112
	buffer_store_dwordx4 v[92:95], v250, s[20:23], s35 offen nt
	ds_write_b128 v173, v[60:63]
	v_pk_fma_f32 v[52:53], v[52:53], v[230:231], v[242:243] op_sel_hi:[1,0,1]
	v_pk_fma_f32 v[54:55], v[54:55], v[230:231], v[244:245] op_sel_hi:[1,0,1]
	v_pk_fma_f32 v[44:45], v[44:45], v[230:231], v[246:247] op_sel_hi:[1,0,1]
	v_pk_fma_f32 v[46:47], v[46:47], v[230:231], v[248:249] op_sel_hi:[1,0,1]
	v_cvt_pk_f16_f32 v52, v52, v53
	v_cvt_pk_f16_f32 v53, v54, v55
	v_cvt_pk_f16_f32 v54, v44, v45
	v_cvt_pk_f16_f32 v55, v46, v47
	ds_write_b128 v173, v[52:55] offset:64
	ds_read_b128 v[108:111], v174
	ds_read_b128 v[100:103], v174 offset:1152
	v_pk_fma_f32 v[48:49], v[48:49], v[230:231], v[234:235] op_sel:[0,1,0]
	v_pk_fma_f32 v[50:51], v[50:51], v[230:231], v[236:237] op_sel:[0,1,0]
	v_pk_fma_f32 v[40:41], v[40:41], v[230:231], v[238:239] op_sel:[0,1,0]
	v_pk_fma_f32 v[42:43], v[42:43], v[230:231], v[240:241] op_sel:[0,1,0]
	v_cvt_pk_f16_f32 v48, v48, v49
	v_cvt_pk_f16_f32 v49, v50, v51
	v_cvt_pk_f16_f32 v50, v40, v41
	v_cvt_pk_f16_f32 v51, v42, v43
	s_waitcnt lgkmcnt(0)
	s_mul_i32 s34, s10, 256
	buffer_store_dwordx4 v[108:111], v250, s[20:23], s34 offen nt
	s_mul_i32 s35, s10, 272
	buffer_store_dwordx4 v[100:103], v250, s[20:23], s35 offen nt
	ds_write_b128 v173, v[48:51]
	v_pk_fma_f32 v[36:37], v[36:37], v[230:231], v[242:243] op_sel:[0,1,0]
	v_pk_fma_f32 v[38:39], v[38:39], v[230:231], v[244:245] op_sel:[0,1,0]
	v_pk_fma_f32 v[28:29], v[28:29], v[230:231], v[246:247] op_sel:[0,1,0]
	v_pk_fma_f32 v[30:31], v[30:31], v[230:231], v[248:249] op_sel:[0,1,0]
	v_cvt_pk_f16_f32 v36, v36, v37
	v_cvt_pk_f16_f32 v37, v38, v39
	v_cvt_pk_f16_f32 v38, v28, v29
	v_cvt_pk_f16_f32 v39, v30, v31
	ds_write_b128 v173, v[36:39] offset:64
	ds_read_b128 v[124:127], v174
	ds_read_b128 v[116:119], v174 offset:1152
	v_pk_fma_f32 v[32:33], v[32:33], v[232:233], v[234:235] op_sel_hi:[1,0,1]
	v_pk_fma_f32 v[34:35], v[34:35], v[232:233], v[236:237] op_sel_hi:[1,0,1]
	v_pk_fma_f32 v[24:25], v[24:25], v[232:233], v[238:239] op_sel_hi:[1,0,1]
	v_pk_fma_f32 v[26:27], v[26:27], v[232:233], v[240:241] op_sel_hi:[1,0,1]
	v_cvt_pk_f16_f32 v32, v32, v33
	v_cvt_pk_f16_f32 v33, v34, v35
	v_cvt_pk_f16_f32 v34, v24, v25
	v_cvt_pk_f16_f32 v35, v26, v27
	ds_write_b128 v173, v[32:35]
	v_pk_fma_f32 v[20:21], v[20:21], v[232:233], v[242:243] op_sel_hi:[1,0,1]
	v_pk_fma_f32 v[22:23], v[22:23], v[232:233], v[244:245] op_sel_hi:[1,0,1]
	v_pk_fma_f32 v[12:13], v[12:13], v[232:233], v[246:247] op_sel_hi:[1,0,1]
	v_pk_fma_f32 v[14:15], v[14:15], v[232:233], v[248:249] op_sel_hi:[1,0,1]
	v_cvt_pk_f16_f32 v20, v20, v21
	v_cvt_pk_f16_f32 v21, v22, v23
	v_cvt_pk_f16_f32 v22, v12, v13
	v_cvt_pk_f16_f32 v23, v14, v15
	ds_write_b128 v173, v[20:23] offset:64
	ds_read_b128 v[88:91], v174
	ds_read_b128 v[76:79], v174 offset:1152
	v_pk_fma_f32 v[16:17], v[16:17], v[232:233], v[234:235] op_sel:[0,1,0]
	v_pk_fma_f32 v[18:19], v[18:19], v[232:233], v[236:237] op_sel:[0,1,0]
	v_pk_fma_f32 v[8:9], v[8:9], v[232:233], v[238:239] op_sel:[0,1,0]
	v_pk_fma_f32 v[10:11], v[10:11], v[232:233], v[240:241] op_sel:[0,1,0]
	v_cvt_pk_f16_f32 v16, v16, v17
	v_cvt_pk_f16_f32 v17, v18, v19
	v_cvt_pk_f16_f32 v18, v8, v9
	v_cvt_pk_f16_f32 v19, v10, v11
	ds_write_b128 v173, v[16:19]
	v_pk_fma_f32 v[4:5], v[4:5], v[232:233], v[242:243] op_sel:[0,1,0]
	v_pk_fma_f32 v[6:7], v[6:7], v[232:233], v[244:245] op_sel:[0,1,0]
	v_pk_fma_f32 v[0:1], v[0:1], v[232:233], v[246:247] op_sel:[0,1,0]
	v_pk_fma_f32 v[2:3], v[2:3], v[232:233], v[248:249] op_sel:[0,1,0]
	v_cvt_pk_f16_f32 v4, v4, v5
	v_cvt_pk_f16_f32 v5, v6, v7
	v_cvt_pk_f16_f32 v6, v0, v1
	v_cvt_pk_f16_f32 v7, v2, v3
	ds_write_b128 v173, v[4:7] offset:64
	ds_read_b128 v[96:99], v174
	ds_read_b128 v[84:87], v174 offset:1152
	s_waitcnt lgkmcnt(0)
	v_mov_b32_e32 v226, v124
	v_mov_b32_e32 v227, v125
	v_mov_b32_e32 v228, v126
	v_mov_b32_e32 v229, v127
	v_mov_b32_e32 v230, v116
	v_mov_b32_e32 v231, v117
	v_mov_b32_e32 v232, v118
	v_mov_b32_e32 v233, v119
	v_mov_b32_e32 v234, v88
	v_mov_b32_e32 v235, v89
	v_mov_b32_e32 v236, v90
	v_mov_b32_e32 v237, v91
	v_mov_b32_e32 v238, v76
	v_mov_b32_e32 v239, v77
	v_mov_b32_e32 v240, v78
	v_mov_b32_e32 v241, v79
	v_mov_b32_e32 v242, v96
	v_mov_b32_e32 v243, v97
	v_mov_b32_e32 v244, v98
	v_mov_b32_e32 v245, v99
	v_mov_b32_e32 v246, v84
	v_mov_b32_e32 v247, v85
	v_mov_b32_e32 v248, v86
	v_mov_b32_e32 v249, v87
	s_mov_b32 s77, 1
	s_mov_b32 s67, s68
	s_mov_b32 s70, s69
	s_mov_b64 s[30:31], s[0:1]
	s_mov_b64 s[28:29], s[8:9]
	s_mov_b64 vcc, s[6:7]
	s_cbranch_vccz .LBB7_12
	s_mul_i32 s78, s10, 288
	buffer_store_dwordx4 v[226:229], v250, s[20:23], s78 offen nt
	s_mul_i32 s78, s10, 304
	buffer_store_dwordx4 v[230:233], v250, s[20:23], s78 offen nt
	s_mul_i32 s78, s10, 320
	buffer_store_dwordx4 v[234:237], v250, s[20:23], s78 offen nt
	s_mul_i32 s78, s10, 336
	buffer_store_dwordx4 v[238:241], v250, s[20:23], s78 offen nt
	s_mul_i32 s78, s10, 352
	buffer_store_dwordx4 v[242:245], v250, s[20:23], s78 offen nt
	s_mul_i32 s78, s10, 368
	buffer_store_dwordx4 v[246:249], v250, s[20:23], s78 offen nt
	s_waitcnt vmcnt(0)
	s_cmpk_gt_u32 s36, 0xff
	s_cbranch_scc1 .LBB7_31
	s_barrier

.LBB7_32:
	s_endpgm
	s_endpgm
	.section	.rodata,"a",@progbits
	.p2align	6, 0x0
	.amdhsa_kernel _Z6k_gemmIN2pg6EpiLinILi0EEELi768EEvNS0_4GemmET_
		.amdhsa_group_segment_fixed_size 0
		.amdhsa_private_segment_fixed_size 0
		.amdhsa_kernarg_size 320
		.amdhsa_user_sgpr_count 2
		.amdhsa_user_sgpr_dispatch_ptr 0
		.amdhsa_user_sgpr_queue_ptr 0
		.amdhsa_user_sgpr_kernarg_segment_ptr 1
		.amdhsa_user_sgpr_dispatch_id 0
		.amdhsa_user_sgpr_kernarg_preload_length 0
		.amdhsa_user_sgpr_kernarg_preload_offset 0
		.amdhsa_user_sgpr_private_segment_size 0
		.amdhsa_uses_dynamic_stack 0
		.amdhsa_enable_private_segment 0
		.amdhsa_system_sgpr_workgroup_id_x 1
		.amdhsa_system_sgpr_workgroup_id_y 0
		.amdhsa_system_sgpr_workgroup_id_z 0
		.amdhsa_system_sgpr_workgroup_info 0
		.amdhsa_system_vgpr_workitem_id 0
		.amdhsa_next_free_vgpr 256
		.amdhsa_next_free_sgpr 80
		.amdhsa_accum_offset 256
		.amdhsa_reserve_vcc 1
		.amdhsa_float_round_mode_32 0
		.amdhsa_float_round_mode_16_64 0
		.amdhsa_float_denorm_mode_32 3
		.amdhsa_float_denorm_mode_16_64 3
		.amdhsa_dx10_clamp 1
		.amdhsa_ieee_mode 1
		.amdhsa_fp16_overflow 0
		.amdhsa_tg_split 0
		.amdhsa_exception_fp_ieee_invalid_op 0
		.amdhsa_exception_fp_denorm_src 0
		.amdhsa_exception_fp_ieee_div_zero 0
		.amdhsa_exception_fp_ieee_overflow 0
		.amdhsa_exception_fp_ieee_underflow 0
		.amdhsa_exception_fp_ieee_inexact 0
		.amdhsa_exception_int_div_zero 0
	.end_amdhsa_kernel

_Z6k_gemmIN2pg6EpiLinILi1EEELi768EEvNS0_4GemmET_:
	s_mov_b32 s77, 0
	s_load_dwordx2 s[4:5], s[0:1], 0x10
	v_readfirstlane_b32 s36, v0
	s_waitcnt lgkmcnt(0)
	s_ashr_i32 s3, s4, 31
	s_ashr_i32 s6, s5, 31
	s_lshr_b32 s3, s3, 24
	s_lshr_b32 s6, s6, 24
	s_add_i32 s3, s4, s3
	s_add_i32 s4, s5, s6
	s_ashr_i32 s3, s3, 8
	s_ashr_i32 s33, s4, 8
	s_mul_i32 s6, s33, s3
	s_cmp_ge_i32 s2, s6
	s_cbranch_scc1 .LBB9_32
	s_ashr_i32 s7, s6, 31
	s_lshr_b32 s4, s7, 29
	s_add_i32 s4, s6, s4
	s_ashr_i32 s37, s4, 3
	s_and_b32 s4, s4, -8
	s_ashr_i32 s39, s2, 31
	s_sub_i32 s38, s6, s4
	s_lshr_b32 s4, s39, 29
	s_add_i32 s10, s2, s4
	s_and_b32 s4, s10, -8
	s_sub_i32 s4, s2, s4
	s_add_i32 s40, s37, 1
	s_cmp_ge_i32 s4, s38
	s_mul_i32 s41, s40, s38
	s_cbranch_scc0 .LBB9_3
	s_sub_i32 s8, s4, s38
	s_mul_i32 s8, s8, s37
	s_add_i32 s11, s8, s41
	s_ashr_i32 s8, s10, 3
	s_cbranch_execz .LBB9_4
	s_branch .LBB9_5

.LBB9_27:
	ds_read_b128 v[128:131], v172
	ds_read_b128 v[132:135], v172 offset:1024
	ds_read_b128 v[136:139], v172 offset:2048
	ds_read_b128 v[140:143], v172 offset:3072
	s_add_u32 s30, s28, 0xfffd0080
	s_addc_u32 s31, s29, -1
	s_cmp_eq_u32 s73, 8
	s_cselect_b32 s35, s9, s31
	s_cselect_b32 s34, s8, s30
	s_cselect_b32 s31, s1, s72
	s_cselect_b32 s30, s0, s71
	v_lshl_add_u64 v[202:203], s[28:29], 0, v[152:153]
	s_add_i32 m0, s43, 0xc000
	ds_read_b128 v[158:161], v173
	ds_read_b128 v[162:165], v173 offset:1024
	ds_read_b128 v[178:181], v173 offset:2048
	ds_read_b128 v[182:185], v173 offset:3072
	ds_read_b128 v[186:189], v173 offset:4096
	ds_read_b128 v[190:193], v173 offset:5120
	ds_read_b128 v[194:197], v173 offset:6144
	ds_read_b128 v[198:201], v173 offset:7168
	global_load_lds_dwordx4 v[202:203], off
	v_lshl_add_u64 v[202:203], s[28:29], 0, v[154:155]
	s_add_i32 m0, s43, 0xe000
	s_nop 0
	global_load_lds_dwordx4 v[202:203], off
	s_waitcnt lgkmcnt(8)
	s_barrier
	s_waitcnt lgkmcnt(0)
	s_setprio 1
	s_waitcnt lgkmcnt(0)
	v_mfma_f32_16x16x32_f16 v[124:127], v[128:131], v[158:161], v[124:127]
	v_mfma_f32_16x16x32_f16 v[120:123], v[136:139], v[158:161], v[120:123]
	v_mfma_f32_16x16x32_f16 v[108:111], v[128:131], v[178:181], v[108:111]
	v_mfma_f32_16x16x32_f16 v[104:107], v[136:139], v[178:181], v[104:107]
	v_mfma_f32_16x16x32_f16 v[96:99], v[128:131], v[186:189], v[96:99]
	v_mfma_f32_16x16x32_f16 v[88:91], v[136:139], v[186:189], v[88:91]
	v_mfma_f32_16x16x32_f16 v[80:83], v[128:131], v[194:197], v[80:83]
	v_mfma_f32_16x16x32_f16 v[72:75], v[136:139], v[194:197], v[72:75]
	v_mfma_f32_16x16x32_f16 v[124:127], v[132:135], v[162:165], v[124:127]
	v_mfma_f32_16x16x32_f16 v[120:123], v[140:143], v[162:165], v[120:123]
	v_mfma_f32_16x16x32_f16 v[108:111], v[132:135], v[182:185], v[108:111]
	v_mfma_f32_16x16x32_f16 v[104:107], v[140:143], v[182:185], v[104:107]
	v_mfma_f32_16x16x32_f16 v[96:99], v[132:135], v[190:193], v[96:99]
	v_mfma_f32_16x16x32_f16 v[88:91], v[140:143], v[190:193], v[88:91]
	v_mfma_f32_16x16x32_f16 v[80:83], v[132:135], v[198:201], v[80:83]
	v_mfma_f32_16x16x32_f16 v[72:75], v[140:143], v[198:201], v[72:75]
	s_setprio 0
	s_barrier
	s_add_i32 s74, s65, s42
	v_lshl_add_u64 v[218:219], s[30:31], 0, v[146:147]
	s_mov_b32 m0, s74
	ds_read_b128 v[202:205], v174
	ds_read_b128 v[206:209], v174 offset:1024
	ds_read_b128 v[210:213], v174 offset:2048
	ds_read_b128 v[214:217], v174 offset:3072
	global_load_lds_dwordx4 v[218:219], off
	v_lshl_add_u64 v[220:221], s[30:31], 0, v[150:151]
	s_add_i32 m0, s74, 0x2000
	s_nop 0
	global_load_lds_dwordx4 v[220:221], off
	s_barrier
	s_waitcnt lgkmcnt(0)
	s_setprio 1
	s_waitcnt lgkmcnt(0)
	v_mfma_f32_16x16x32_f16 v[116:119], v[202:205], v[158:161], v[116:119]
	v_mfma_f32_16x16x32_f16 v[112:115], v[210:213], v[158:161], v[112:115]
	v_mfma_f32_16x16x32_f16 v[100:103], v[202:205], v[178:181], v[100:103]
	v_mfma_f32_16x16x32_f16 v[92:95], v[210:213], v[178:181], v[92:95]
	v_mfma_f32_16x16x32_f16 v[84:87], v[202:205], v[186:189], v[84:87]
	v_mfma_f32_16x16x32_f16 v[76:79], v[210:213], v[186:189], v[76:79]
	v_mfma_f32_16x16x32_f16 v[68:71], v[202:205], v[194:197], v[68:71]
	v_mfma_f32_16x16x32_f16 v[64:67], v[210:213], v[194:197], v[64:67]
	v_mfma_f32_16x16x32_f16 v[116:119], v[206:209], v[162:165], v[116:119]
	v_mfma_f32_16x16x32_f16 v[112:115], v[214:217], v[162:165], v[112:115]
	v_mfma_f32_16x16x32_f16 v[100:103], v[206:209], v[182:185], v[100:103]
	v_mfma_f32_16x16x32_f16 v[92:95], v[214:217], v[182:185], v[92:95]
	v_mfma_f32_16x16x32_f16 v[84:87], v[206:209], v[190:193], v[84:87]
	v_mfma_f32_16x16x32_f16 v[76:79], v[214:217], v[190:193], v[76:79]
	v_mfma_f32_16x16x32_f16 v[68:71], v[206:209], v[198:201], v[68:71]
	v_mfma_f32_16x16x32_f16 v[64:67], v[214:217], v[198:201], v[64:67]
	s_setprio 0
	s_mov_b32 m0, s43
	v_lshl_add_u64 v[222:223], s[34:35], 0, v[144:145]
	s_barrier
	ds_read_b128 v[158:161], v173 offset:16384
	ds_read_b128 v[162:165], v173 offset:17408
	ds_read_b128 v[178:181], v173 offset:18432
	ds_read_b128 v[182:185], v173 offset:19456
	ds_read_b128 v[186:189], v173 offset:20480
	ds_read_b128 v[190:193], v173 offset:21504
	ds_read_b128 v[194:197], v173 offset:22528
	ds_read_b128 v[198:201], v173 offset:23552
	global_load_lds_dwordx4 v[222:223], off
	v_lshl_add_u64 v[224:225], s[34:35], 0, v[148:149]
	s_mov_b32 m0, s44
	s_nop 0
	global_load_lds_dwordx4 v[224:225], off
	s_barrier
	s_waitcnt lgkmcnt(0)
	s_setprio 1
	s_waitcnt lgkmcnt(0)
	v_mfma_f32_16x16x32_f16 v[60:63], v[128:131], v[158:161], v[60:63]
	v_mfma_f32_16x16x32_f16 v[56:59], v[136:139], v[158:161], v[56:59]
	v_mfma_f32_16x16x32_f16 v[48:51], v[128:131], v[178:181], v[48:51]
	v_mfma_f32_16x16x32_f16 v[40:43], v[136:139], v[178:181], v[40:43]
	v_mfma_f32_16x16x32_f16 v[32:35], v[128:131], v[186:189], v[32:35]
	v_mfma_f32_16x16x32_f16 v[24:27], v[136:139], v[186:189], v[24:27]
	v_mfma_f32_16x16x32_f16 v[16:19], v[128:131], v[194:197], v[16:19]
	v_mfma_f32_16x16x32_f16 v[8:11], v[136:139], v[194:197], v[8:11]
	v_mfma_f32_16x16x32_f16 v[60:63], v[132:135], v[162:165], v[60:63]
	v_mfma_f32_16x16x32_f16 v[56:59], v[140:143], v[162:165], v[56:59]
	v_mfma_f32_16x16x32_f16 v[48:51], v[132:135], v[182:185], v[48:51]
	v_mfma_f32_16x16x32_f16 v[40:43], v[140:143], v[182:185], v[40:43]
	v_mfma_f32_16x16x32_f16 v[32:35], v[132:135], v[190:193], v[32:35]
	v_mfma_f32_16x16x32_f16 v[24:27], v[140:143], v[190:193], v[24:27]
	v_mfma_f32_16x16x32_f16 v[16:19], v[132:135], v[198:201], v[16:19]
	v_mfma_f32_16x16x32_f16 v[8:11], v[140:143], v[198:201], v[8:11]
	s_setprio 0
	s_barrier
	s_add_u32 s74, s30, 0xc000
	s_addc_u32 s75, s31, 0
	s_add_i32 s76, s66, s42
	v_lshl_add_u64 v[128:129], s[74:75], 0, v[146:147]
	s_mov_b32 m0, s76
	s_nop 0
	global_load_lds_dwordx4 v[128:129], off
	v_lshl_add_u64 v[128:129], s[74:75], 0, v[150:151]
	s_add_i32 m0, s76, 0x2000
	s_nop 0
	global_load_lds_dwordx4 v[128:129], off
	s_waitcnt vmcnt(6)
	s_cmp_eq_u32 s77, 0
	s_cbranch_scc1 .Ldef9_a
	s_mul_i32 s78, s10, 288
	buffer_store_dwordx4 v[226:229], v250, s[20:23], s78 offen nt
	s_mul_i32 s78, s10, 304
	buffer_store_dwordx4 v[230:233], v250, s[20:23], s78 offen nt
	s_mul_i32 s78, s10, 320
	buffer_store_dwordx4 v[234:237], v250, s[20:23], s78 offen nt
.Ldef9_a:
	s_barrier
	s_setprio 1
	v_mfma_f32_16x16x32_f16 v[52:55], v[202:205], v[158:161], v[52:55]
	v_mfma_f32_16x16x32_f16 v[44:47], v[210:213], v[158:161], v[44:47]
	v_mfma_f32_16x16x32_f16 v[36:39], v[202:205], v[178:181], v[36:39]
	v_mfma_f32_16x16x32_f16 v[28:31], v[210:213], v[178:181], v[28:31]
	v_mfma_f32_16x16x32_f16 v[20:23], v[202:205], v[186:189], v[20:23]
	v_mfma_f32_16x16x32_f16 v[12:15], v[210:213], v[186:189], v[12:15]
	v_mfma_f32_16x16x32_f16 v[4:7], v[202:205], v[194:197], v[4:7]
	v_mfma_f32_16x16x32_f16 v[0:3], v[210:213], v[194:197], v[0:3]
	v_mfma_f32_16x16x32_f16 v[52:55], v[206:209], v[162:165], v[52:55]
	v_mfma_f32_16x16x32_f16 v[44:47], v[214:217], v[162:165], v[44:47]
	v_mfma_f32_16x16x32_f16 v[36:39], v[206:209], v[182:185], v[36:39]
	v_mfma_f32_16x16x32_f16 v[28:31], v[214:217], v[182:185], v[28:31]
	v_mfma_f32_16x16x32_f16 v[20:23], v[206:209], v[190:193], v[20:23]
	v_mfma_f32_16x16x32_f16 v[12:15], v[214:217], v[190:193], v[12:15]
	v_mfma_f32_16x16x32_f16 v[4:7], v[206:209], v[198:201], v[4:7]
	v_mfma_f32_16x16x32_f16 v[0:3], v[214:217], v[198:201], v[0:3]
	s_setprio 0
	s_add_i32 s74, 0, 0x18000
	v_add_u32_e32 v140, s74, v168
	s_barrier
	ds_read_b128 v[128:131], v140
	ds_read_b128 v[132:135], v140 offset:1024
	ds_read_b128 v[136:139], v140 offset:2048
	ds_read_b128 v[140:143], v140 offset:3072
	s_add_u32 s34, s34, 0x30000
	s_addc_u32 s35, s35, 0
	s_mov_b32 m0, s45
	v_lshl_add_u64 v[202:203], s[34:35], 0, v[144:145]
	ds_read_b128 v[158:161], v173 offset:32768
	ds_read_b128 v[162:165], v173 offset:33792
	ds_read_b128 v[178:181], v173 offset:34816
	ds_read_b128 v[182:185], v173 offset:35840
	ds_read_b128 v[186:189], v173 offset:36864
	ds_read_b128 v[190:193], v173 offset:37888
	ds_read_b128 v[194:197], v173 offset:38912
	ds_read_b128 v[198:201], v173 offset:39936
	global_load_lds_dwordx4 v[202:203], off
	v_lshl_add_u64 v[202:203], s[34:35], 0, v[148:149]
	s_mov_b32 m0, s46
	s_nop 0
	global_load_lds_dwordx4 v[202:203], off
	s_cmp_eq_u32 s73, 8
	s_cbranch_scc0 .Lpf9_skip
	s_lshl_b32 s78, s70, 8
	s_add_i32 s78, s78, s48
	v_or_b32_e32 v252, s78, v167
	v_ashrrev_i32_e32 v253, 31, v252
	v_lshl_add_u64 v[252:253], v[252:253], 3, s[12:13]
	s_lshl_b32 s79, s68, 8
	s_or_b32 s79, s79, s51
	v_or_b32_e32 v254, s79, v166
	v_ashrrev_i32_e32 v255, 31, v254
	v_lshl_add_u64 v[254:255], v[254:255], 2, s[14:15]
	global_load_dword v226, v[252:253], off offset:4
	global_load_dword v227, v[252:253], off offset:132
	global_load_dword v228, v[252:253], off offset:260
	global_load_dword v229, v[252:253], off offset:388
	global_load_dword v230, v[252:253], off offset:1028
	global_load_dword v231, v[252:253], off offset:1156
	global_load_dword v232, v[252:253], off offset:1284
	global_load_dword v233, v[252:253], off offset:1412
	global_load_dwordx4 v[234:237], v[254:255], off
	global_load_dwordx4 v[238:241], v[254:255], off offset:16
	global_load_dwordx4 v[242:245], v[254:255], off offset:128
	global_load_dwordx4 v[246:249], v[254:255], off offset:144
.Lpf9_skip:
	s_waitcnt lgkmcnt(8)
	s_barrier
	s_waitcnt lgkmcnt(0)
	s_setprio 1
	s_waitcnt lgkmcnt(0)
	v_mfma_f32_16x16x32_f16 v[124:127], v[128:131], v[158:161], v[124:127]
	v_mfma_f32_16x16x32_f16 v[120:123], v[136:139], v[158:161], v[120:123]
	v_mfma_f32_16x16x32_f16 v[108:111], v[128:131], v[178:181], v[108:111]
	v_mfma_f32_16x16x32_f16 v[104:107], v[136:139], v[178:181], v[104:107]
	v_mfma_f32_16x16x32_f16 v[96:99], v[128:131], v[186:189], v[96:99]
	v_mfma_f32_16x16x32_f16 v[88:91], v[136:139], v[186:189], v[88:91]
	v_mfma_f32_16x16x32_f16 v[80:83], v[128:131], v[194:197], v[80:83]
	v_mfma_f32_16x16x32_f16 v[72:75], v[136:139], v[194:197], v[72:75]
	v_mfma_f32_16x16x32_f16 v[124:127], v[132:135], v[162:165], v[124:127]
	v_mfma_f32_16x16x32_f16 v[120:123], v[140:143], v[162:165], v[120:123]
	v_mfma_f32_16x16x32_f16 v[108:111], v[132:135], v[182:185], v[108:111]
	v_mfma_f32_16x16x32_f16 v[104:107], v[140:143], v[182:185], v[104:107]
	v_mfma_f32_16x16x32_f16 v[96:99], v[132:135], v[190:193], v[96:99]
	v_mfma_f32_16x16x32_f16 v[88:91], v[140:143], v[190:193], v[88:91]
	v_mfma_f32_16x16x32_f16 v[80:83], v[132:135], v[198:201], v[80:83]
	v_mfma_f32_16x16x32_f16 v[72:75], v[140:143], v[198:201], v[72:75]
	s_setprio 0
	s_barrier
	s_add_i32 s34, 0, 0x1c000
	s_add_i32 s35, s74, s42
	v_add_u32_e32 v177, s34, v168
	v_lshl_add_u64 v[218:219], v[218:219], 0, s[26:27]
	s_mov_b32 m0, s35
	ds_read_b128 v[202:205], v177
	ds_read_b128 v[206:209], v177 offset:1024
	ds_read_b128 v[210:213], v177 offset:2048
	ds_read_b128 v[214:217], v177 offset:3072
	global_load_lds_dwordx4 v[218:219], off
	v_lshl_add_u64 v[218:219], v[220:221], 0, s[26:27]
	s_add_i32 m0, s35, 0x2000
	s_nop 0
	global_load_lds_dwordx4 v[218:219], off
	s_barrier
	s_waitcnt lgkmcnt(0)
	s_setprio 1
	s_waitcnt lgkmcnt(0)
	v_mfma_f32_16x16x32_f16 v[116:119], v[202:205], v[158:161], v[116:119]
	v_mfma_f32_16x16x32_f16 v[112:115], v[210:213], v[158:161], v[112:115]
	v_mfma_f32_16x16x32_f16 v[100:103], v[202:205], v[178:181], v[100:103]
	v_mfma_f32_16x16x32_f16 v[92:95], v[210:213], v[178:181], v[92:95]
	v_mfma_f32_16x16x32_f16 v[84:87], v[202:205], v[186:189], v[84:87]
	v_mfma_f32_16x16x32_f16 v[76:79], v[210:213], v[186:189], v[76:79]
	v_mfma_f32_16x16x32_f16 v[68:71], v[202:205], v[194:197], v[68:71]
	v_mfma_f32_16x16x32_f16 v[64:67], v[210:213], v[194:197], v[64:67]
	v_mfma_f32_16x16x32_f16 v[116:119], v[206:209], v[162:165], v[116:119]
	v_mfma_f32_16x16x32_f16 v[112:115], v[214:217], v[162:165], v[112:115]
	v_mfma_f32_16x16x32_f16 v[100:103], v[206:209], v[182:185], v[100:103]
	v_mfma_f32_16x16x32_f16 v[92:95], v[214:217], v[182:185], v[92:95]
	v_mfma_f32_16x16x32_f16 v[84:87], v[206:209], v[190:193], v[84:87]
	v_mfma_f32_16x16x32_f16 v[76:79], v[214:217], v[190:193], v[76:79]
	v_mfma_f32_16x16x32_f16 v[68:71], v[206:209], v[198:201], v[68:71]
	v_mfma_f32_16x16x32_f16 v[64:67], v[214:217], v[198:201], v[64:67]
	s_setprio 0
	s_mov_b32 m0, s49
	v_lshl_add_u64 v[218:219], v[222:223], 0, s[26:27]
	s_barrier
	ds_read_b128 v[158:161], v173 offset:49152
	ds_read_b128 v[162:165], v173 offset:50176
	ds_read_b128 v[178:181], v173 offset:51200
	ds_read_b128 v[182:185], v173 offset:52224
	ds_read_b128 v[186:189], v173 offset:53248
	ds_read_b128 v[190:193], v173 offset:54272
	ds_read_b128 v[194:197], v173 offset:55296
	ds_read_b128 v[198:201], v173 offset:56320
	global_load_lds_dwordx4 v[218:219], off
	v_lshl_add_u64 v[218:219], v[224:225], 0, s[26:27]
	s_mov_b32 m0, s50
	s_nop 0
	global_load_lds_dwordx4 v[218:219], off
	s_barrier
	s_waitcnt lgkmcnt(0)
	s_setprio 1
	s_waitcnt lgkmcnt(0)
	v_mfma_f32_16x16x32_f16 v[60:63], v[128:131], v[158:161], v[60:63]
	v_mfma_f32_16x16x32_f16 v[56:59], v[136:139], v[158:161], v[56:59]
	v_mfma_f32_16x16x32_f16 v[48:51], v[128:131], v[178:181], v[48:51]
	v_mfma_f32_16x16x32_f16 v[40:43], v[136:139], v[178:181], v[40:43]
	v_mfma_f32_16x16x32_f16 v[32:35], v[128:131], v[186:189], v[32:35]
	v_mfma_f32_16x16x32_f16 v[24:27], v[136:139], v[186:189], v[24:27]
	v_mfma_f32_16x16x32_f16 v[16:19], v[128:131], v[194:197], v[16:19]
	v_mfma_f32_16x16x32_f16 v[8:11], v[136:139], v[194:197], v[8:11]
	v_mfma_f32_16x16x32_f16 v[60:63], v[132:135], v[162:165], v[60:63]
	v_mfma_f32_16x16x32_f16 v[56:59], v[140:143], v[162:165], v[56:59]
	v_mfma_f32_16x16x32_f16 v[48:51], v[132:135], v[182:185], v[48:51]
	v_mfma_f32_16x16x32_f16 v[40:43], v[140:143], v[182:185], v[40:43]
	v_mfma_f32_16x16x32_f16 v[32:35], v[132:135], v[190:193], v[32:35]
	v_mfma_f32_16x16x32_f16 v[24:27], v[140:143], v[190:193], v[24:27]
	v_mfma_f32_16x16x32_f16 v[16:19], v[132:135], v[198:201], v[16:19]
	v_mfma_f32_16x16x32_f16 v[8:11], v[140:143], v[198:201], v[8:11]
	s_setprio 0
	s_barrier
	s_add_u32 s30, s30, 0xc080
	s_addc_u32 s31, s31, 0
	s_add_i32 s34, s34, s42
	v_lshl_add_u64 v[128:129], s[30:31], 0, v[146:147]
	s_mov_b32 m0, s34
	s_nop 0
	global_load_lds_dwordx4 v[128:129], off
	v_lshl_add_u64 v[128:129], s[30:31], 0, v[150:151]
	s_add_i32 m0, s34, 0x2000
	s_nop 0
	global_load_lds_dwordx4 v[128:129], off
	s_cmp_eq_u32 s73, 8
	s_cbranch_scc1 .Lw89_last
	s_waitcnt vmcnt(6)
	s_branch .Lw89_j

.Ldef9_b:
	s_barrier
	s_setprio 1
	v_mfma_f32_16x16x32_f16 v[52:55], v[202:205], v[158:161], v[52:55]
	v_mfma_f32_16x16x32_f16 v[44:47], v[210:213], v[158:161], v[44:47]
	v_mfma_f32_16x16x32_f16 v[36:39], v[202:205], v[178:181], v[36:39]
	v_mfma_f32_16x16x32_f16 v[28:31], v[210:213], v[178:181], v[28:31]
	v_mfma_f32_16x16x32_f16 v[20:23], v[202:205], v[186:189], v[20:23]
	v_mfma_f32_16x16x32_f16 v[12:15], v[210:213], v[186:189], v[12:15]
	v_mfma_f32_16x16x32_f16 v[4:7], v[202:205], v[194:197], v[4:7]
	v_mfma_f32_16x16x32_f16 v[0:3], v[210:213], v[194:197], v[0:3]
	v_mfma_f32_16x16x32_f16 v[52:55], v[206:209], v[162:165], v[52:55]
	v_mfma_f32_16x16x32_f16 v[44:47], v[214:217], v[162:165], v[44:47]
	v_mfma_f32_16x16x32_f16 v[36:39], v[206:209], v[182:185], v[36:39]
	v_mfma_f32_16x16x32_f16 v[28:31], v[214:217], v[182:185], v[28:31]
	v_mfma_f32_16x16x32_f16 v[20:23], v[206:209], v[190:193], v[20:23]
	v_mfma_f32_16x16x32_f16 v[12:15], v[214:217], v[190:193], v[12:15]
	v_mfma_f32_16x16x32_f16 v[4:7], v[206:209], v[198:201], v[4:7]
	v_mfma_f32_16x16x32_f16 v[0:3], v[214:217], v[198:201], v[0:3]
	s_setprio 0
	s_add_i32 s73, s73, 2
	s_add_u32 s28, s28, 0x100
	s_addc_u32 s29, s29, 0
	s_add_u32 s71, s71, 0x100
	s_addc_u32 s72, s72, 0
	s_cmp_gt_u32 s73, 9
	s_barrier
	s_cbranch_scc0 .LBB9_27
	s_lshl_b32 s28, s70, 8
	s_add_i32 s28, s28, s48
	s_lshl_b32 s29, s68, 8
	s_or_b32 s29, s29, s51
	s_waitcnt vmcnt(6)
	v_pk_fma_f32 v[124:125], v[124:125], v[226:227], v[234:235] op_sel_hi:[1,0,1]
	v_pk_fma_f32 v[126:127], v[126:127], v[226:227], v[236:237] op_sel_hi:[1,0,1]
	v_pk_fma_f32 v[120:121], v[120:121], v[226:227], v[238:239] op_sel_hi:[1,0,1]
	v_pk_fma_f32 v[122:123], v[122:123], v[226:227], v[240:241] op_sel_hi:[1,0,1]
	v_cvt_pk_f16_f32 v124, v124, v125
	v_cvt_pk_f16_f32 v125, v126, v127
	v_cvt_pk_f16_f32 v126, v120, v121
	v_cvt_pk_f16_f32 v127, v122, v123
	v_pk_max_f16 v124, v124, 0
	v_pk_max_f16 v125, v125, 0
	v_pk_max_f16 v126, v126, 0
	v_pk_max_f16 v127, v127, 0
	v_add_u32_e32 v250, s28, v169
	v_mul_lo_u32 v250, v250, s10
	v_add_u32_e32 v250, s29, v250
	v_lshl_add_u32 v250, v250, 1, v170
	ds_write_b128 v175, v[124:127]
	v_pk_fma_f32 v[116:117], v[116:117], v[226:227], v[242:243] op_sel_hi:[1,0,1]
	v_pk_fma_f32 v[118:119], v[118:119], v[226:227], v[244:245] op_sel_hi:[1,0,1]
	v_pk_fma_f32 v[112:113], v[112:113], v[226:227], v[246:247] op_sel_hi:[1,0,1]
	v_pk_fma_f32 v[114:115], v[114:115], v[226:227], v[248:249] op_sel_hi:[1,0,1]
	v_cvt_pk_f16_f32 v116, v116, v117
	v_cvt_pk_f16_f32 v117, v118, v119
	v_cvt_pk_f16_f32 v118, v112, v113
	v_cvt_pk_f16_f32 v119, v114, v115
	v_pk_max_f16 v116, v116, 0
	v_pk_max_f16 v117, v117, 0
	v_pk_max_f16 v118, v118, 0
	v_pk_max_f16 v119, v119, 0
	ds_write_b128 v175, v[116:119] offset:64
	ds_read_b128 v[120:123], v176
	ds_read_b128 v[112:115], v176 offset:1152
	v_pk_fma_f32 v[108:109], v[108:109], v[226:227], v[234:235] op_sel:[0,1,0]
	v_pk_fma_f32 v[110:111], v[110:111], v[226:227], v[236:237] op_sel:[0,1,0]
	v_pk_fma_f32 v[104:105], v[104:105], v[226:227], v[238:239] op_sel:[0,1,0]
	v_pk_fma_f32 v[106:107], v[106:107], v[226:227], v[240:241] op_sel:[0,1,0]
	v_cvt_pk_f16_f32 v108, v108, v109
	v_cvt_pk_f16_f32 v109, v110, v111
	v_cvt_pk_f16_f32 v110, v104, v105
	v_cvt_pk_f16_f32 v111, v106, v107
	v_pk_max_f16 v108, v108, 0
	v_pk_max_f16 v109, v109, 0
	v_pk_max_f16 v110, v110, 0
	v_pk_max_f16 v111, v111, 0
	s_waitcnt lgkmcnt(0)
	s_mul_i32 s34, s10, 0
	buffer_store_dwordx4 v[120:123], v250, s[20:23], s34 offen nt
	s_mul_i32 s35, s10, 16
	buffer_store_dwordx4 v[112:115], v250, s[20:23], s35 offen nt
	ds_write_b128 v175, v[108:111]
	v_pk_fma_f32 v[100:101], v[100:101], v[226:227], v[242:243] op_sel:[0,1,0]
	v_pk_fma_f32 v[102:103], v[102:103], v[226:227], v[244:245] op_sel:[0,1,0]
	v_pk_fma_f32 v[92:93], v[92:93], v[226:227], v[246:247] op_sel:[0,1,0]
	v_pk_fma_f32 v[94:95], v[94:95], v[226:227], v[248:249] op_sel:[0,1,0]
	v_cvt_pk_f16_f32 v100, v100, v101
	v_cvt_pk_f16_f32 v101, v102, v103
	v_cvt_pk_f16_f32 v102, v92, v93
	v_cvt_pk_f16_f32 v103, v94, v95
	v_pk_max_f16 v100, v100, 0
	v_pk_max_f16 v101, v101, 0
	v_pk_max_f16 v102, v102, 0
	v_pk_max_f16 v103, v103, 0
	ds_write_b128 v175, v[100:103] offset:64
	ds_read_b128 v[124:127], v176
	ds_read_b128 v[116:119], v176 offset:1152
	v_pk_fma_f32 v[96:97], v[96:97], v[228:229], v[234:235] op_sel_hi:[1,0,1]
	v_pk_fma_f32 v[98:99], v[98:99], v[228:229], v[236:237] op_sel_hi:[1,0,1]
	v_pk_fma_f32 v[88:89], v[88:89], v[228:229], v[238:239] op_sel_hi:[1,0,1]
	v_pk_fma_f32 v[90:91], v[90:91], v[228:229], v[240:241] op_sel_hi:[1,0,1]
	v_cvt_pk_f16_f32 v96, v96, v97
	v_cvt_pk_f16_f32 v97, v98, v99
	v_cvt_pk_f16_f32 v98, v88, v89
	v_cvt_pk_f16_f32 v99, v90, v91
	v_pk_max_f16 v96, v96, 0
	v_pk_max_f16 v97, v97, 0
	v_pk_max_f16 v98, v98, 0
	v_pk_max_f16 v99, v99, 0
	s_waitcnt lgkmcnt(0)
	s_mul_i32 s34, s10, 32
	buffer_store_dwordx4 v[124:127], v250, s[20:23], s34 offen nt
	s_mul_i32 s35, s10, 48
	buffer_store_dwordx4 v[116:119], v250, s[20:23], s35 offen nt
	ds_write_b128 v175, v[96:99]
	v_pk_fma_f32 v[84:85], v[84:85], v[228:229], v[242:243] op_sel_hi:[1,0,1]
	v_pk_fma_f32 v[86:87], v[86:87], v[228:229], v[244:245] op_sel_hi:[1,0,1]
	v_pk_fma_f32 v[76:77], v[76:77], v[228:229], v[246:247] op_sel_hi:[1,0,1]
	v_pk_fma_f32 v[78:79], v[78:79], v[228:229], v[248:249] op_sel_hi:[1,0,1]
	v_cvt_pk_f16_f32 v84, v84, v85
	v_cvt_pk_f16_f32 v85, v86, v87
	v_cvt_pk_f16_f32 v86, v76, v77
	v_cvt_pk_f16_f32 v87, v78, v79
	v_pk_max_f16 v84, v84, 0
	v_pk_max_f16 v85, v85, 0
	v_pk_max_f16 v86, v86, 0
	v_pk_max_f16 v87, v87, 0
	ds_write_b128 v175, v[84:87] offset:64
	ds_read_b128 v[120:123], v176
	ds_read_b128 v[112:115], v176 offset:1152
	v_pk_fma_f32 v[80:81], v[80:81], v[228:229], v[234:235] op_sel:[0,1,0]
	v_pk_fma_f32 v[82:83], v[82:83], v[228:229], v[236:237] op_sel:[0,1,0]
	v_pk_fma_f32 v[72:73], v[72:73], v[228:229], v[238:239] op_sel:[0,1,0]
	v_pk_fma_f32 v[74:75], v[74:75], v[228:229], v[240:241] op_sel:[0,1,0]
	v_cvt_pk_f16_f32 v80, v80, v81
	v_cvt_pk_f16_f32 v81, v82, v83
	v_cvt_pk_f16_f32 v82, v72, v73
	v_cvt_pk_f16_f32 v83, v74, v75
	v_pk_max_f16 v80, v80, 0
	v_pk_max_f16 v81, v81, 0
	v_pk_max_f16 v82, v82, 0
	v_pk_max_f16 v83, v83, 0
	s_waitcnt lgkmcnt(0)
	s_mul_i32 s34, s10, 64
	buffer_store_dwordx4 v[120:123], v250, s[20:23], s34 offen nt
	s_mul_i32 s35, s10, 80
	buffer_store_dwordx4 v[112:115], v250, s[20:23], s35 offen nt
	ds_write_b128 v175, v[80:83]
	v_pk_fma_f32 v[68:69], v[68:69], v[228:229], v[242:243] op_sel:[0,1,0]
	v_pk_fma_f32 v[70:71], v[70:71], v[228:229], v[244:245] op_sel:[0,1,0]
	v_pk_fma_f32 v[64:65], v[64:65], v[228:229], v[246:247] op_sel:[0,1,0]
	v_pk_fma_f32 v[66:67], v[66:67], v[228:229], v[248:249] op_sel:[0,1,0]
	v_cvt_pk_f16_f32 v68, v68, v69
	v_cvt_pk_f16_f32 v69, v70, v71
	v_cvt_pk_f16_f32 v70, v64, v65
	v_cvt_pk_f16_f32 v71, v66, v67
	v_pk_max_f16 v68, v68, 0
	v_pk_max_f16 v69, v69, 0
	v_pk_max_f16 v70, v70, 0
	v_pk_max_f16 v71, v71, 0
	ds_write_b128 v175, v[68:71] offset:64
	ds_read_b128 v[104:107], v176
	ds_read_b128 v[92:95], v176 offset:1152
	v_pk_fma_f32 v[60:61], v[60:61], v[230:231], v[234:235] op_sel_hi:[1,0,1]
	v_pk_fma_f32 v[62:63], v[62:63], v[230:231], v[236:237] op_sel_hi:[1,0,1]
	v_pk_fma_f32 v[56:57], v[56:57], v[230:231], v[238:239] op_sel_hi:[1,0,1]
	v_pk_fma_f32 v[58:59], v[58:59], v[230:231], v[240:241] op_sel_hi:[1,0,1]
	v_cvt_pk_f16_f32 v60, v60, v61
	v_cvt_pk_f16_f32 v61, v62, v63
	v_cvt_pk_f16_f32 v62, v56, v57
	v_cvt_pk_f16_f32 v63, v58, v59
	v_pk_max_f16 v60, v60, 0
	v_pk_max_f16 v61, v61, 0
	v_pk_max_f16 v62, v62, 0
	v_pk_max_f16 v63, v63, 0
	s_waitcnt lgkmcnt(0)
	s_mul_i32 s34, s10, 96
	buffer_store_dwordx4 v[104:107], v250, s[20:23], s34 offen nt
	s_mul_i32 s35, s10, 112
	buffer_store_dwordx4 v[92:95], v250, s[20:23], s35 offen nt
	ds_write_b128 v175, v[60:63]
	v_pk_fma_f32 v[52:53], v[52:53], v[230:231], v[242:243] op_sel_hi:[1,0,1]
	v_pk_fma_f32 v[54:55], v[54:55], v[230:231], v[244:245] op_sel_hi:[1,0,1]
	v_pk_fma_f32 v[44:45], v[44:45], v[230:231], v[246:247] op_sel_hi:[1,0,1]
	v_pk_fma_f32 v[46:47], v[46:47], v[230:231], v[248:249] op_sel_hi:[1,0,1]
	v_cvt_pk_f16_f32 v52, v52, v53
	v_cvt_pk_f16_f32 v53, v54, v55
	v_cvt_pk_f16_f32 v54, v44, v45
	v_cvt_pk_f16_f32 v55, v46, v47
	v_pk_max_f16 v52, v52, 0
	v_pk_max_f16 v53, v53, 0
	v_pk_max_f16 v54, v54, 0
	v_pk_max_f16 v55, v55, 0
	ds_write_b128 v175, v[52:55] offset:64
	ds_read_b128 v[108:111], v176
	ds_read_b128 v[100:103], v176 offset:1152
	v_pk_fma_f32 v[48:49], v[48:49], v[230:231], v[234:235] op_sel:[0,1,0]
	v_pk_fma_f32 v[50:51], v[50:51], v[230:231], v[236:237] op_sel:[0,1,0]
	v_pk_fma_f32 v[40:41], v[40:41], v[230:231], v[238:239] op_sel:[0,1,0]
	v_pk_fma_f32 v[42:43], v[42:43], v[230:231], v[240:241] op_sel:[0,1,0]
	v_cvt_pk_f16_f32 v48, v48, v49
	v_cvt_pk_f16_f32 v49, v50, v51
	v_cvt_pk_f16_f32 v50, v40, v41
	v_cvt_pk_f16_f32 v51, v42, v43
	v_pk_max_f16 v48, v48, 0
	v_pk_max_f16 v49, v49, 0
	v_pk_max_f16 v50, v50, 0
	v_pk_max_f16 v51, v51, 0
	s_waitcnt lgkmcnt(0)
	s_mul_i32 s34, s10, 256
	buffer_store_dwordx4 v[108:111], v250, s[20:23], s34 offen nt
	s_mul_i32 s35, s10, 272
	buffer_store_dwordx4 v[100:103], v250, s[20:23], s35 offen nt
	ds_write_b128 v175, v[48:51]
	v_pk_fma_f32 v[36:37], v[36:37], v[230:231], v[242:243] op_sel:[0,1,0]
	v_pk_fma_f32 v[38:39], v[38:39], v[230:231], v[244:245] op_sel:[0,1,0]
	v_pk_fma_f32 v[28:29], v[28:29], v[230:231], v[246:247] op_sel:[0,1,0]
	v_pk_fma_f32 v[30:31], v[30:31], v[230:231], v[248:249] op_sel:[0,1,0]
	v_cvt_pk_f16_f32 v36, v36, v37
	v_cvt_pk_f16_f32 v37, v38, v39
	v_cvt_pk_f16_f32 v38, v28, v29
	v_cvt_pk_f16_f32 v39, v30, v31
	v_pk_max_f16 v36, v36, 0
	v_pk_max_f16 v37, v37, 0
	v_pk_max_f16 v38, v38, 0
	v_pk_max_f16 v39, v39, 0
	ds_write_b128 v175, v[36:39] offset:64
	ds_read_b128 v[124:127], v176
	ds_read_b128 v[116:119], v176 offset:1152
	v_pk_fma_f32 v[32:33], v[32:33], v[232:233], v[234:235] op_sel_hi:[1,0,1]
	v_pk_fma_f32 v[34:35], v[34:35], v[232:233], v[236:237] op_sel_hi:[1,0,1]
	v_pk_fma_f32 v[24:25], v[24:25], v[232:233], v[238:239] op_sel_hi:[1,0,1]
	v_pk_fma_f32 v[26:27], v[26:27], v[232:233], v[240:241] op_sel_hi:[1,0,1]
	v_cvt_pk_f16_f32 v32, v32, v33
	v_cvt_pk_f16_f32 v33, v34, v35
	v_cvt_pk_f16_f32 v34, v24, v25
	v_cvt_pk_f16_f32 v35, v26, v27
	v_pk_max_f16 v32, v32, 0
	v_pk_max_f16 v33, v33, 0
	v_pk_max_f16 v34, v34, 0
	v_pk_max_f16 v35, v35, 0
	ds_write_b128 v175, v[32:35]
	v_pk_fma_f32 v[20:21], v[20:21], v[232:233], v[242:243] op_sel_hi:[1,0,1]
	v_pk_fma_f32 v[22:23], v[22:23], v[232:233], v[244:245] op_sel_hi:[1,0,1]
	v_pk_fma_f32 v[12:13], v[12:13], v[232:233], v[246:247] op_sel_hi:[1,0,1]
	v_pk_fma_f32 v[14:15], v[14:15], v[232:233], v[248:249] op_sel_hi:[1,0,1]
	v_cvt_pk_f16_f32 v20, v20, v21
	v_cvt_pk_f16_f32 v21, v22, v23
	v_cvt_pk_f16_f32 v22, v12, v13
	v_cvt_pk_f16_f32 v23, v14, v15
	v_pk_max_f16 v20, v20, 0
	v_pk_max_f16 v21, v21, 0
	v_pk_max_f16 v22, v22, 0
	v_pk_max_f16 v23, v23, 0
	ds_write_b128 v175, v[20:23] offset:64
	ds_read_b128 v[88:91], v176
	ds_read_b128 v[76:79], v176 offset:1152
	v_pk_fma_f32 v[16:17], v[16:17], v[232:233], v[234:235] op_sel:[0,1,0]
	v_pk_fma_f32 v[18:19], v[18:19], v[232:233], v[236:237] op_sel:[0,1,0]
	v_pk_fma_f32 v[8:9], v[8:9], v[232:233], v[238:239] op_sel:[0,1,0]
	v_pk_fma_f32 v[10:11], v[10:11], v[232:233], v[240:241] op_sel:[0,1,0]
	v_cvt_pk_f16_f32 v16, v16, v17
	v_cvt_pk_f16_f32 v17, v18, v19
	v_cvt_pk_f16_f32 v18, v8, v9
	v_cvt_pk_f16_f32 v19, v10, v11
	v_pk_max_f16 v16, v16, 0
	v_pk_max_f16 v17, v17, 0
	v_pk_max_f16 v18, v18, 0
	v_pk_max_f16 v19, v19, 0
	ds_write_b128 v175, v[16:19]
	v_pk_fma_f32 v[4:5], v[4:5], v[232:233], v[242:243] op_sel:[0,1,0]
	v_pk_fma_f32 v[6:7], v[6:7], v[232:233], v[244:245] op_sel:[0,1,0]
	v_pk_fma_f32 v[0:1], v[0:1], v[232:233], v[246:247] op_sel:[0,1,0]
	v_pk_fma_f32 v[2:3], v[2:3], v[232:233], v[248:249] op_sel:[0,1,0]
	v_cvt_pk_f16_f32 v4, v4, v5
	v_cvt_pk_f16_f32 v5, v6, v7
	v_cvt_pk_f16_f32 v6, v0, v1
	v_cvt_pk_f16_f32 v7, v2, v3
	v_pk_max_f16 v4, v4, 0
	v_pk_max_f16 v5, v5, 0
	v_pk_max_f16 v6, v6, 0
	v_pk_max_f16 v7, v7, 0
	ds_write_b128 v175, v[4:7] offset:64
	ds_read_b128 v[96:99], v176
	ds_read_b128 v[84:87], v176 offset:1152
	s_waitcnt lgkmcnt(0)
	v_mov_b32_e32 v226, v124
	v_mov_b32_e32 v227, v125
	v_mov_b32_e32 v228, v126
	v_mov_b32_e32 v229, v127
	v_mov_b32_e32 v230, v116
	v_mov_b32_e32 v231, v117
	v_mov_b32_e32 v232, v118
	v_mov_b32_e32 v233, v119
	v_mov_b32_e32 v234, v88
	v_mov_b32_e32 v235, v89
	v_mov_b32_e32 v236, v90
	v_mov_b32_e32 v237, v91
	v_mov_b32_e32 v238, v76
	v_mov_b32_e32 v239, v77
	v_mov_b32_e32 v240, v78
	v_mov_b32_e32 v241, v79
	v_mov_b32_e32 v242, v96
	v_mov_b32_e32 v243, v97
	v_mov_b32_e32 v244, v98
	v_mov_b32_e32 v245, v99
	v_mov_b32_e32 v246, v84
	v_mov_b32_e32 v247, v85
	v_mov_b32_e32 v248, v86
	v_mov_b32_e32 v249, v87
	s_mov_b32 s77, 1
	s_mov_b32 s68, s67
	s_mov_b32 s70, s69
	s_mov_b64 s[30:31], s[0:1]
	s_mov_b64 s[28:29], s[8:9]
	s_mov_b64 vcc, s[6:7]
	s_cbranch_vccz .LBB9_12
	s_mul_i32 s78, s10, 288
	buffer_store_dwordx4 v[226:229], v250, s[20:23], s78 offen nt
	s_mul_i32 s78, s10, 304
	buffer_store_dwordx4 v[230:233], v250, s[20:23], s78 offen nt
	s_mul_i32 s78, s10, 320
	buffer_store_dwordx4 v[234:237], v250, s[20:23], s78 offen nt
	s_mul_i32 s78, s10, 336
	buffer_store_dwordx4 v[238:241], v250, s[20:23], s78 offen nt
	s_mul_i32 s78, s10, 352
	buffer_store_dwordx4 v[242:245], v250, s[20:23], s78 offen nt
	s_mul_i32 s78, s10, 368
	buffer_store_dwordx4 v[246:249], v250, s[20:23], s78 offen nt
	s_waitcnt vmcnt(0)
	s_cmpk_gt_u32 s36, 0xff
	s_cbranch_scc1 .LBB9_31
	s_barrier

.LBB9_32:
	s_endpgm
	s_endpgm
	.section	.rodata,"a",@progbits
	.p2align	6, 0x0
	.amdhsa_kernel _Z6k_gemmIN2pg6EpiLinILi1EEELi768EEvNS0_4GemmET_
		.amdhsa_group_segment_fixed_size 0
		.amdhsa_private_segment_fixed_size 0
		.amdhsa_kernarg_size 320
		.amdhsa_user_sgpr_count 2
		.amdhsa_user_sgpr_dispatch_ptr 0
		.amdhsa_user_sgpr_queue_ptr 0
		.amdhsa_user_sgpr_kernarg_segment_ptr 1
		.amdhsa_user_sgpr_dispatch_id 0
		.amdhsa_user_sgpr_kernarg_preload_length 0
		.amdhsa_user_sgpr_kernarg_preload_offset 0
		.amdhsa_user_sgpr_private_segment_size 0
		.amdhsa_uses_dynamic_stack 0
		.amdhsa_enable_private_segment 0
		.amdhsa_system_sgpr_workgroup_id_x 1
		.amdhsa_system_sgpr_workgroup_id_y 0
		.amdhsa_system_sgpr_workgroup_id_z 0
		.amdhsa_system_sgpr_workgroup_info 0
		.amdhsa_system_vgpr_workitem_id 0
		.amdhsa_next_free_vgpr 256
		.amdhsa_next_free_sgpr 80
		.amdhsa_accum_offset 256
		.amdhsa_reserve_vcc 1
		.amdhsa_float_round_mode_32 0
		.amdhsa_float_round_mode_16_64 0
		.amdhsa_float_denorm_mode_32 3
		.amdhsa_float_denorm_mode_16_64 3
		.amdhsa_dx10_clamp 1
		.amdhsa_ieee_mode 1
		.amdhsa_fp16_overflow 0
		.amdhsa_tg_split 0
		.amdhsa_exception_fp_ieee_invalid_op 0
		.amdhsa_exception_fp_denorm_src 0
		.amdhsa_exception_fp_ieee_div_zero 0
		.amdhsa_exception_fp_ieee_overflow 0
		.amdhsa_exception_fp_ieee_underflow 0
		.amdhsa_exception_fp_ieee_inexact 0
		.amdhsa_exception_int_div_zero 0
	.end_amdhsa_kernel

amdhsa.kernels:
  - .agpr_count:     16
    .args:
      - .actual_access:  read_only
        .address_space:  global
        .offset:         0
        .size:           8
        .value_kind:     global_buffer
      - .actual_access:  read_only
        .address_space:  global
        .offset:         8
        .size:           8
        .value_kind:     global_buffer
      - .actual_access:  write_only
        .address_space:  global
        .offset:         16
        .size:           8
        .value_kind:     global_buffer
    .group_segment_fixed_size: 45056
    .kernarg_segment_align: 8
    .kernarg_segment_size: 24
    .language:       OpenCL C
    .language_version:
      - 2
      - 0
    .max_flat_workgroup_size: 256
    .name:           _Z6k_attnPKDF16_PKfPDF16_
    .private_segment_fixed_size: 0
    .sgpr_count:     16
    .sgpr_spill_count: 0
    .symbol:         _Z6k_attnPKDF16_PKfPDF16_.kd
    .uniform_work_group_size: 1
    .uses_dynamic_stack: false
    .vgpr_count:     84
    .vgpr_spill_count: 0
    .wavefront_size: 64
  - .agpr_count:     0
    .args:
      - .actual_access:  read_only
        .address_space:  global
        .offset:         0
        .size:           8
        .value_kind:     global_buffer
      - .actual_access:  read_only
        .address_space:  global
        .offset:         8
        .size:           8
        .value_kind:     global_buffer
      - .actual_access:  write_only
        .address_space:  global
        .offset:         16
        .size:           8
        .value_kind:     global_buffer
      - .actual_access:  write_only
        .address_space:  global
        .offset:         24
        .size:           8
        .value_kind:     global_buffer
      - .actual_access:  write_only
        .address_space:  global
        .offset:         32
        .size:           8
        .value_kind:     global_buffer
      - .actual_access:  write_only
        .address_space:  global
        .offset:         40
        .size:           8
        .value_kind:     global_buffer
    .group_segment_fixed_size: 0
    .kernarg_segment_align: 8
    .kernarg_segment_size: 48
    .language:       OpenCL C
    .language_version:
      - 2
      - 0
    .max_flat_workgroup_size: 256
    .name:           _Z11k_prep_miscPKiPKfPfPDv2_fS3_S3_
    .private_segment_fixed_size: 0
    .sgpr_count:     16
    .sgpr_spill_count: 0
    .symbol:         _Z11k_prep_miscPKiPKfPfPDv2_fS3_S3_.kd
    .uniform_work_group_size: 1
    .uses_dynamic_stack: false
    .vgpr_count:     6
    .vgpr_spill_count: 0
    .wavefront_size: 64
  - .agpr_count:     0
    .args:
      - .actual_access:  read_only
        .address_space:  global
        .offset:         0
        .size:           8
        .value_kind:     global_buffer
      - .actual_access:  write_only
        .address_space:  global
        .offset:         8
        .size:           8
        .value_kind:     global_buffer
    .group_segment_fixed_size: 0
    .kernarg_segment_align: 8
    .kernarg_segment_size: 16
    .language:       OpenCL C
    .language_version:
      - 2
      - 0
    .max_flat_workgroup_size: 256
    .name:           _Z7k_cvt_xPKfPDF16_
    .private_segment_fixed_size: 0
    .sgpr_count:     14
    .sgpr_spill_count: 0
    .symbol:         _Z7k_cvt_xPKfPDF16_.kd
    .uniform_work_group_size: 1
    .uses_dynamic_stack: false
    .vgpr_count:     12
    .vgpr_spill_count: 0
    .wavefront_size: 64
  - .agpr_count:     0
    .args:
      - .offset:         0
        .size:           176
        .value_kind:     by_value
    .group_segment_fixed_size: 9216
    .kernarg_segment_align: 8
    .kernarg_segment_size: 176
    .language:       OpenCL C
    .language_version:
      - 2
      - 0
    .max_flat_workgroup_size: 256
    .name:           _Z8k_wtrans8PrepArgs
    .private_segment_fixed_size: 0
    .sgpr_count:     44
    .sgpr_spill_count: 0
    .symbol:         _Z8k_wtrans8PrepArgs.kd
    .uniform_work_group_size: 1
    .uses_dynamic_stack: false
    .vgpr_count:     18
    .vgpr_spill_count: 0
    .wavefront_size: 64
  - .agpr_count:     0
    .args:
      - .offset:         0
        .size:           176
        .value_kind:     by_value
      - .actual_access:  read_only
        .address_space:  global
        .offset:         176
        .size:           8
        .value_kind:     global_buffer
      - .actual_access:  read_only
        .address_space:  global
        .offset:         184
        .size:           8
        .value_kind:     global_buffer
    .group_segment_fixed_size: 2048
    .kernarg_segment_align: 8
    .kernarg_segment_size: 192
    .language:       OpenCL C
    .language_version:
      - 2
      - 0
    .max_flat_workgroup_size: 256
    .name:           _Z8k_colvec8PrepArgsPKfS1_
    .private_segment_fixed_size: 0
    .sgpr_count:     38
    .sgpr_spill_count: 0
    .symbol:         _Z8k_colvec8PrepArgsPKfS1_.kd
    .uniform_work_group_size: 1
    .uses_dynamic_stack: false
    .vgpr_count:     114
    .vgpr_spill_count: 0
    .wavefront_size: 64
  - .agpr_count:     0
    .args:
      - .actual_access:  read_only
        .address_space:  global
        .offset:         0
        .size:           8
        .value_kind:     global_buffer
      - .actual_access:  write_only
        .address_space:  global
        .offset:         8
        .size:           8
        .value_kind:     global_buffer
    .group_segment_fixed_size: 0
    .kernarg_segment_align: 8
    .kernarg_segment_size: 16
    .language:       OpenCL C
    .language_version:
      - 2
      - 0
    .max_flat_workgroup_size: 256
    .name:           _Z9k_rowstatPKDv2_fPS_
    .private_segment_fixed_size: 0
    .sgpr_count:     16
    .sgpr_spill_count: 0
    .symbol:         _Z9k_rowstatPKDv2_fPS_.kd
    .uniform_work_group_size: 1
    .uses_dynamic_stack: false
    .vgpr_count:     28
    .vgpr_spill_count: 0
    .wavefront_size: 64
  - .agpr_count:     0
    .args:
      - .actual_access:  read_only
        .address_space:  global
        .offset:         0
        .size:           8
        .value_kind:     global_buffer
      - .actual_access:  read_only
        .address_space:  global
        .offset:         8
        .size:           8
        .value_kind:     global_buffer
      - .actual_access:  read_only
        .address_space:  global
        .offset:         16
        .size:           8
        .value_kind:     global_buffer
      - .actual_access:  read_only
        .address_space:  global
        .offset:         24
        .size:           8
        .value_kind:     global_buffer
      - .actual_access:  write_only
        .address_space:  global
        .offset:         32
        .size:           8
        .value_kind:     global_buffer
    .group_segment_fixed_size: 0
    .kernarg_segment_align: 8
    .kernarg_segment_size: 40
    .language:       OpenCL C
    .language_version:
      - 2
      - 0
    .max_flat_workgroup_size: 256
    .name:           _Z10k_final_lnPKDF16_PKDv2_fPKfS5_Pf
    .private_segment_fixed_size: 0
    .sgpr_count:     19
    .sgpr_spill_count: 0
    .symbol:         _Z10k_final_lnPKDF16_PKDv2_fPKfS5_Pf.kd
    .uniform_work_group_size: 1
    .uses_dynamic_stack: false
    .vgpr_count:     19
    .vgpr_spill_count: 0
    .wavefront_size: 64
  - .agpr_count:     0
    .args:
      - .offset:         0
        .size:           32
        .value_kind:     by_value
      - .offset:         32
        .size:           32
        .value_kind:     by_value
      - .offset:         64
        .size:           4
        .value_kind:     hidden_block_count_x
      - .offset:         68
        .size:           4
        .value_kind:     hidden_block_count_y
      - .offset:         72
        .size:           4
        .value_kind:     hidden_block_count_z
      - .offset:         76
        .size:           2
        .value_kind:     hidden_group_size_x
      - .offset:         78
        .size:           2
        .value_kind:     hidden_group_size_y
      - .offset:         80
        .size:           2
        .value_kind:     hidden_group_size_z
      - .offset:         82
        .size:           2
        .value_kind:     hidden_remainder_x
      - .offset:         84
        .size:           2
        .value_kind:     hidden_remainder_y
      - .offset:         86
        .size:           2
        .value_kind:     hidden_remainder_z
      - .offset:         104
        .size:           8
        .value_kind:     hidden_global_offset_x
      - .offset:         112
        .size:           8
        .value_kind:     hidden_global_offset_y
      - .offset:         120
        .size:           8
        .value_kind:     hidden_global_offset_z
      - .offset:         128
        .size:           2
        .value_kind:     hidden_grid_dims
      - .offset:         184
        .size:           4
        .value_kind:     hidden_dynamic_lds_size
    .group_segment_fixed_size: 0
    .kernarg_segment_align: 8
    .kernarg_segment_size: 320
    .language:       OpenCL C
    .language_version:
      - 2
      - 0
    .max_flat_workgroup_size: 512
    .name:           _Z6k_gemmIN2pg6EpiLinILi0EEELi768EEvNS0_4GemmET_
    .private_segment_fixed_size: 0
    .sgpr_count:     86
    .sgpr_spill_count: 0
    .symbol:         _Z6k_gemmIN2pg6EpiLinILi0EEELi768EEvNS0_4GemmET_.kd
    .uniform_work_group_size: 1
    .uses_dynamic_stack: false
    .vgpr_count:     256
    .vgpr_spill_count: 0
    .wavefront_size: 64
  - .agpr_count:     0
    .args:
      - .offset:         0
        .size:           32
        .value_kind:     by_value
      - .offset:         32
        .size:           56
        .value_kind:     by_value
      - .offset:         88
        .size:           4
        .value_kind:     hidden_block_count_x
      - .offset:         92
        .size:           4
        .value_kind:     hidden_block_count_y
      - .offset:         96
        .size:           4
        .value_kind:     hidden_block_count_z
      - .offset:         100
        .size:           2
        .value_kind:     hidden_group_size_x
      - .offset:         102
        .size:           2
        .value_kind:     hidden_group_size_y
      - .offset:         104
        .size:           2
        .value_kind:     hidden_group_size_z
      - .offset:         106
        .size:           2
        .value_kind:     hidden_remainder_x
      - .offset:         108
        .size:           2
        .value_kind:     hidden_remainder_y
      - .offset:         110
        .size:           2
        .value_kind:     hidden_remainder_z
      - .offset:         128
        .size:           8
        .value_kind:     hidden_global_offset_x
      - .offset:         136
        .size:           8
        .value_kind:     hidden_global_offset_y
      - .offset:         144
        .size:           8
        .value_kind:     hidden_global_offset_z
      - .offset:         152
        .size:           2
        .value_kind:     hidden_grid_dims
      - .offset:         208
        .size:           4
        .value_kind:     hidden_dynamic_lds_size
    .group_segment_fixed_size: 0
    .kernarg_segment_align: 8
    .kernarg_segment_size: 344
    .language:       OpenCL C
    .language_version:
      - 2
      - 0
    .max_flat_workgroup_size: 512
    .name:           _Z6k_gemmIN2pg6EpiResELi768EEvNS0_4GemmET_
    .private_segment_fixed_size: 0
    .sgpr_count:     108
    .sgpr_spill_count: 0
    .symbol:         _Z6k_gemmIN2pg6EpiResELi768EEvNS0_4GemmET_.kd
    .uniform_work_group_size: 1
    .uses_dynamic_stack: false
    .vgpr_count:     256
    .vgpr_spill_count: 0
    .wavefront_size: 64
  - .agpr_count:     0
    .args:
      - .offset:         0
        .size:           32
        .value_kind:     by_value
      - .offset:         32
        .size:           32
        .value_kind:     by_value
      - .offset:         64
        .size:           4
        .value_kind:     hidden_block_count_x
      - .offset:         68
        .size:           4
        .value_kind:     hidden_block_count_y
      - .offset:         72
        .size:           4
        .value_kind:     hidden_block_count_z
      - .offset:         76
        .size:           2
        .value_kind:     hidden_group_size_x
      - .offset:         78
        .size:           2
        .value_kind:     hidden_group_size_y
      - .offset:         80
        .size:           2
        .value_kind:     hidden_group_size_z
      - .offset:         82
        .size:           2
        .value_kind:     hidden_remainder_x
      - .offset:         84
        .size:           2
        .value_kind:     hidden_remainder_y
      - .offset:         86
        .size:           2
        .value_kind:     hidden_remainder_z
      - .offset:         104
        .size:           8
        .value_kind:     hidden_global_offset_x
      - .offset:         112
        .size:           8
        .value_kind:     hidden_global_offset_y
      - .offset:         120
        .size:           8
        .value_kind:     hidden_global_offset_z
      - .offset:         128
        .size:           2
        .value_kind:     hidden_grid_dims
      - .offset:         184
        .size:           4
        .value_kind:     hidden_dynamic_lds_size
    .group_segment_fixed_size: 0
    .kernarg_segment_align: 8
    .kernarg_segment_size: 320
    .language:       OpenCL C
    .language_version:
      - 2
      - 0
    .max_flat_workgroup_size: 512
    .name:           _Z6k_gemmIN2pg6EpiLinILi1EEELi768EEvNS0_4GemmET_
    .private_segment_fixed_size: 0
    .sgpr_count:     86
    .sgpr_spill_count: 0
    .symbol:         _Z6k_gemmIN2pg6EpiLinILi1EEELi768EEvNS0_4GemmET_.kd
    .uniform_work_group_size: 1
    .uses_dynamic_stack: false
    .vgpr_count:     256
    .vgpr_spill_count: 0
    .wavefront_size: 64
  - .agpr_count:     0
    .args:
      - .offset:         0
        .size:           32
        .value_kind:     by_value
      - .offset:         32
        .size:           56
        .value_kind:     by_value
      - .offset:         88
        .size:           4
        .value_kind:     hidden_block_count_x
      - .offset:         92
        .size:           4
        .value_kind:     hidden_block_count_y
      - .offset:         96
        .size:           4
        .value_kind:     hidden_block_count_z
      - .offset:         100
        .size:           2
        .value_kind:     hidden_group_size_x
      - .offset:         102
        .size:           2
        .value_kind:     hidden_group_size_y
      - .offset:         104
        .size:           2
        .value_kind:     hidden_group_size_z
      - .offset:         106
        .size:           2
        .value_kind:     hidden_remainder_x
      - .offset:         108
        .size:           2
        .value_kind:     hidden_remainder_y
      - .offset:         110
        .size:           2
        .value_kind:     hidden_remainder_z
      - .offset:         128
        .size:           8
        .value_kind:     hidden_global_offset_x
      - .offset:         136
        .size:           8
        .value_kind:     hidden_global_offset_y
      - .offset:         144
        .size:           8
        .value_kind:     hidden_global_offset_z
      - .offset:         152
        .size:           2
        .value_kind:     hidden_grid_dims
      - .offset:         208
        .size:           4
        .value_kind:     hidden_dynamic_lds_size
    .group_segment_fixed_size: 0
    .kernarg_segment_align: 8
    .kernarg_segment_size: 344
    .language:       OpenCL C
    .language_version:
      - 2
      - 0
    .max_flat_workgroup_size: 512
    .name:           _Z6k_gemmIN2pg6EpiResELi3072EEvNS0_4GemmET_
    .private_segment_fixed_size: 0
    .sgpr_count:     108
    .sgpr_spill_count: 0
    .symbol:         _Z6k_gemmIN2pg6EpiResELi3072EEvNS0_4GemmET_.kd
    .uniform_work_group_size: 1
    .uses_dynamic_stack: false
    .vgpr_count:     256
    .vgpr_spill_count: 0
    .wavefront_size: 64
